# on top of the XCD-contiguous MoE order: in six GEMM K-loops the LDS-DMA issues of each load segment move ahead of the segment's ds_reads (legal reorder inside one barrier epoch)
# baseline (speedup 1.0000x reference)
.LBB0_130:
	s_add_u32 s4, s38, 0x80
	s_addc_u32 s5, s39, 0
	s_add_i32 s31, 0, 0x10000
	s_cmp_eq_u32 s29, 28
	s_cselect_b32 s5, s35, s5
	s_cselect_b32 s4, s34, s4
	s_cselect_b32 s43, s37, s15
	s_cselect_b32 s42, s36, s14
	s_add_i32 s68, 0, 0x14000
	v_lshl_add_u64 v[146:147], s[38:39], 0, v[144:145]
	s_add_i32 m0, s48, 0xc000
	s_nop 0
	global_load_lds_dwordx4 v[146:147], off
	v_lshl_add_u64 v[146:147], s[38:39], 0, v[142:143]
	s_add_i32 m0, s48, 0xe000
	s_nop 0
	global_load_lds_dwordx4 v[146:147], off
	v_add_u32_e32 v146, s31, v148
	ds_read_b128 v[152:155], v146
	ds_read_b128 v[156:159], v146 offset:1024
	ds_read_b128 v[160:163], v146 offset:2048
	ds_read_b128 v[164:167], v146 offset:3072
	v_add_u32_e32 v146, s68, v148
	ds_read_b128 v[168:171], v146
	ds_read_b128 v[172:175], v146 offset:1024
	ds_read_b128 v[176:179], v146 offset:2048
	ds_read_b128 v[180:183], v146 offset:3072
	ds_read_b128 v[184:187], v150
	ds_read_b128 v[188:191], v150 offset:1024
	ds_read_b128 v[192:195], v150 offset:2048
	ds_read_b128 v[196:199], v150 offset:3072
	ds_read_b128 v[224:227], v150 offset:4096
	ds_read_b128 v[228:231], v150 offset:5120
	ds_read_b128 v[238:241], v150 offset:6144
	ds_read_b128 v[242:245], v150 offset:7168
	s_waitcnt vmcnt(8)
	s_waitcnt lgkmcnt(0)
	s_barrier
	s_setprio 1
	s_waitcnt lgkmcnt(0)
	v_mfma_f32_16x16x32_bf16 v[128:131], v[152:155], v[184:187], v[128:131]
	v_mfma_f32_16x16x32_bf16 v[124:127], v[160:163], v[184:187], v[124:127]
	v_mfma_f32_16x16x32_bf16 v[120:123], v[152:155], v[192:195], v[120:123]
	v_mfma_f32_16x16x32_bf16 v[112:115], v[160:163], v[192:195], v[112:115]
	v_mfma_f32_16x16x32_bf16 v[104:107], v[152:155], v[224:227], v[104:107]
	v_mfma_f32_16x16x32_bf16 v[96:99], v[160:163], v[224:227], v[96:99]
	v_mfma_f32_16x16x32_bf16 v[88:91], v[152:155], v[238:241], v[88:91]
	v_mfma_f32_16x16x32_bf16 v[80:83], v[160:163], v[238:241], v[80:83]
	v_mfma_f32_16x16x32_bf16 v[128:131], v[156:159], v[188:191], v[128:131]
	v_mfma_f32_16x16x32_bf16 v[124:127], v[164:167], v[188:191], v[124:127]
	v_mfma_f32_16x16x32_bf16 v[120:123], v[156:159], v[196:199], v[120:123]
	v_mfma_f32_16x16x32_bf16 v[112:115], v[164:167], v[196:199], v[112:115]
	v_mfma_f32_16x16x32_bf16 v[104:107], v[156:159], v[228:231], v[104:107]
	v_mfma_f32_16x16x32_bf16 v[96:99], v[164:167], v[228:231], v[96:99]
	v_mfma_f32_16x16x32_bf16 v[88:91], v[156:159], v[242:245], v[88:91]
	v_mfma_f32_16x16x32_bf16 v[80:83], v[164:167], v[242:245], v[80:83]
	s_setprio 0
	s_setprio 1
	v_mfma_f32_16x16x32_bf16 v[116:119], v[168:171], v[184:187], v[116:119]
	v_mfma_f32_16x16x32_bf16 v[108:111], v[176:179], v[184:187], v[108:111]
	v_mfma_f32_16x16x32_bf16 v[100:103], v[168:171], v[192:195], v[100:103]
	v_mfma_f32_16x16x32_bf16 v[92:95], v[176:179], v[192:195], v[92:95]
	v_mfma_f32_16x16x32_bf16 v[84:87], v[168:171], v[224:227], v[84:87]
	v_mfma_f32_16x16x32_bf16 v[76:79], v[176:179], v[224:227], v[76:79]
	v_mfma_f32_16x16x32_bf16 v[72:75], v[168:171], v[238:241], v[72:75]
	v_mfma_f32_16x16x32_bf16 v[68:71], v[176:179], v[238:241], v[68:71]
	v_mfma_f32_16x16x32_bf16 v[116:119], v[172:175], v[188:191], v[116:119]
	v_mfma_f32_16x16x32_bf16 v[108:111], v[180:183], v[188:191], v[108:111]
	v_mfma_f32_16x16x32_bf16 v[100:103], v[172:175], v[196:199], v[100:103]
	v_mfma_f32_16x16x32_bf16 v[92:95], v[180:183], v[196:199], v[92:95]
	v_mfma_f32_16x16x32_bf16 v[84:87], v[172:175], v[228:231], v[84:87]
	v_mfma_f32_16x16x32_bf16 v[76:79], v[180:183], v[228:231], v[76:79]
	v_mfma_f32_16x16x32_bf16 v[72:75], v[172:175], v[242:245], v[72:75]
	v_mfma_f32_16x16x32_bf16 v[68:71], v[180:183], v[242:245], v[68:71]
	s_setprio 0
	s_barrier
	s_add_i32 s31, s31, s47
	v_lshl_add_u64 v[146:147], s[42:43], 0, v[34:35]
	s_mov_b32 m0, s31
	s_nop 0
	global_load_lds_dwordx4 v[146:147], off
	s_add_i32 m0, s31, 0x2000
	s_add_u32 s64, s42, 0x80000
	v_lshl_add_u64 v[212:213], s[42:43], 0, v[132:133]
	s_addc_u32 s65, s43, 0
	s_add_i32 s31, s68, s47
	global_load_lds_dwordx4 v[212:213], off
	v_lshl_add_u64 v[232:233], s[64:65], 0, v[34:35]
	s_mov_b32 m0, s31
	v_lshl_add_u64 v[246:247], s[4:5], 0, v[134:135]
	global_load_lds_dwordx4 v[232:233], off
	v_lshl_add_u64 v[232:233], s[64:65], 0, v[132:133]
	s_add_i32 m0, s31, 0x2000
	s_nop 0
	global_load_lds_dwordx4 v[232:233], off
	v_lshl_add_u64 v[232:233], s[4:5], 0, v[138:139]
	s_mov_b32 m0, s48
	s_nop 0
	global_load_lds_dwordx4 v[232:233], off
	s_mov_b32 m0, s49
	s_nop 0
	global_load_lds_dwordx4 v[246:247], off
	ds_read_b128 v[184:187], v150 offset:16384
	ds_read_b128 v[188:191], v150 offset:17408
	ds_read_b128 v[192:195], v150 offset:18432
	ds_read_b128 v[196:199], v150 offset:19456
	ds_read_b128 v[224:227], v150 offset:20480
	ds_read_b128 v[228:231], v150 offset:21504
	ds_read_b128 v[238:241], v150 offset:22528
	ds_read_b128 v[242:245], v150 offset:23552
	s_waitcnt vmcnt(8)
	s_waitcnt lgkmcnt(0)
	s_barrier
	s_setprio 1
	s_waitcnt lgkmcnt(0)
	v_mfma_f32_16x16x32_bf16 v[64:67], v[152:155], v[184:187], v[64:67]
	v_mfma_f32_16x16x32_bf16 v[60:63], v[160:163], v[184:187], v[60:63]
	v_mfma_f32_16x16x32_bf16 v[52:55], v[152:155], v[192:195], v[52:55]
	v_mfma_f32_16x16x32_bf16 v[44:47], v[160:163], v[192:195], v[44:47]
	v_mfma_f32_16x16x32_bf16 v[36:39], v[152:155], v[224:227], v[36:39]
	v_mfma_f32_16x16x32_bf16 v[26:29], v[160:163], v[224:227], v[26:29]
	v_mfma_f32_16x16x32_bf16 v[18:21], v[152:155], v[238:241], v[18:21]
	v_mfma_f32_16x16x32_bf16 v[10:13], v[160:163], v[238:241], v[10:13]
	v_mfma_f32_16x16x32_bf16 v[64:67], v[156:159], v[188:191], v[64:67]
	v_mfma_f32_16x16x32_bf16 v[60:63], v[164:167], v[188:191], v[60:63]
	v_mfma_f32_16x16x32_bf16 v[52:55], v[156:159], v[196:199], v[52:55]
	v_mfma_f32_16x16x32_bf16 v[44:47], v[164:167], v[196:199], v[44:47]
	v_mfma_f32_16x16x32_bf16 v[36:39], v[156:159], v[228:231], v[36:39]
	v_mfma_f32_16x16x32_bf16 v[26:29], v[164:167], v[228:231], v[26:29]
	v_mfma_f32_16x16x32_bf16 v[18:21], v[156:159], v[242:245], v[18:21]
	v_mfma_f32_16x16x32_bf16 v[10:13], v[164:167], v[242:245], v[10:13]
	s_setprio 0
	s_setprio 1
	v_mfma_f32_16x16x32_bf16 v[56:59], v[168:171], v[184:187], v[56:59]
	v_mfma_f32_16x16x32_bf16 v[48:51], v[176:179], v[184:187], v[48:51]
	v_mfma_f32_16x16x32_bf16 v[40:43], v[168:171], v[192:195], v[40:43]
	v_mfma_f32_16x16x32_bf16 v[30:33], v[176:179], v[192:195], v[30:33]
	v_mfma_f32_16x16x32_bf16 v[22:25], v[168:171], v[224:227], v[22:25]
	v_mfma_f32_16x16x32_bf16 v[14:17], v[176:179], v[224:227], v[14:17]
	v_mfma_f32_16x16x32_bf16 v[6:9], v[168:171], v[238:241], v[6:9]
	v_mfma_f32_16x16x32_bf16 v[2:5], v[176:179], v[238:241], v[2:5]
	v_mfma_f32_16x16x32_bf16 v[56:59], v[172:175], v[188:191], v[56:59]
	v_mfma_f32_16x16x32_bf16 v[48:51], v[180:183], v[188:191], v[48:51]
	v_mfma_f32_16x16x32_bf16 v[40:43], v[172:175], v[196:199], v[40:43]
	v_mfma_f32_16x16x32_bf16 v[30:33], v[180:183], v[196:199], v[30:33]
	v_mfma_f32_16x16x32_bf16 v[22:25], v[172:175], v[228:231], v[22:25]
	v_mfma_f32_16x16x32_bf16 v[14:17], v[180:183], v[228:231], v[14:17]
	v_mfma_f32_16x16x32_bf16 v[6:9], v[172:175], v[242:245], v[6:9]
	v_mfma_f32_16x16x32_bf16 v[2:5], v[180:183], v[242:245], v[2:5]
	s_setprio 0
	s_barrier
	s_add_i32 s31, 0, 0x18000
	s_add_i32 s64, 0, 0x1c000
	s_mov_b32 m0, s50
	v_lshl_add_u64 v[248:249], s[4:5], 0, v[140:141]
	global_load_lds_dwordx4 v[248:249], off
	v_lshl_add_u64 v[248:249], s[4:5], 0, v[136:137]
	s_mov_b32 m0, s51
	s_nop 0
	global_load_lds_dwordx4 v[248:249], off
	v_add_u32_e32 v151, s31, v148
	ds_read_b128 v[152:155], v151
	ds_read_b128 v[156:159], v151 offset:1024
	ds_read_b128 v[160:163], v151 offset:2048
	ds_read_b128 v[164:167], v151 offset:3072
	v_add_u32_e32 v151, s64, v148
	ds_read_b128 v[168:171], v151
	ds_read_b128 v[172:175], v151 offset:1024
	ds_read_b128 v[176:179], v151 offset:2048
	ds_read_b128 v[180:183], v151 offset:3072
	ds_read_b128 v[184:187], v150 offset:32768
	ds_read_b128 v[188:191], v150 offset:33792
	ds_read_b128 v[192:195], v150 offset:34816
	ds_read_b128 v[196:199], v150 offset:35840
	ds_read_b128 v[224:227], v150 offset:36864
	ds_read_b128 v[228:231], v150 offset:37888
	ds_read_b128 v[238:241], v150 offset:38912
	ds_read_b128 v[242:245], v150 offset:39936
	s_waitcnt vmcnt(8)
	s_waitcnt lgkmcnt(0)
	s_barrier
	s_setprio 1
	s_waitcnt lgkmcnt(0)
	v_mfma_f32_16x16x32_bf16 v[128:131], v[152:155], v[184:187], v[128:131]
	v_mfma_f32_16x16x32_bf16 v[124:127], v[160:163], v[184:187], v[124:127]
	v_mfma_f32_16x16x32_bf16 v[120:123], v[152:155], v[192:195], v[120:123]
	v_mfma_f32_16x16x32_bf16 v[112:115], v[160:163], v[192:195], v[112:115]
	v_mfma_f32_16x16x32_bf16 v[104:107], v[152:155], v[224:227], v[104:107]
	v_mfma_f32_16x16x32_bf16 v[96:99], v[160:163], v[224:227], v[96:99]
	v_mfma_f32_16x16x32_bf16 v[88:91], v[152:155], v[238:241], v[88:91]
	v_mfma_f32_16x16x32_bf16 v[80:83], v[160:163], v[238:241], v[80:83]
	v_mfma_f32_16x16x32_bf16 v[128:131], v[156:159], v[188:191], v[128:131]
	v_mfma_f32_16x16x32_bf16 v[124:127], v[164:167], v[188:191], v[124:127]
	v_mfma_f32_16x16x32_bf16 v[120:123], v[156:159], v[196:199], v[120:123]
	v_mfma_f32_16x16x32_bf16 v[112:115], v[164:167], v[196:199], v[112:115]
	v_mfma_f32_16x16x32_bf16 v[104:107], v[156:159], v[228:231], v[104:107]
	v_mfma_f32_16x16x32_bf16 v[96:99], v[164:167], v[228:231], v[96:99]
	v_mfma_f32_16x16x32_bf16 v[88:91], v[156:159], v[242:245], v[88:91]
	v_mfma_f32_16x16x32_bf16 v[80:83], v[164:167], v[242:245], v[80:83]
	s_setprio 0
	s_setprio 1
	v_mfma_f32_16x16x32_bf16 v[116:119], v[168:171], v[184:187], v[116:119]
	v_mfma_f32_16x16x32_bf16 v[108:111], v[176:179], v[184:187], v[108:111]
	v_mfma_f32_16x16x32_bf16 v[100:103], v[168:171], v[192:195], v[100:103]
	v_mfma_f32_16x16x32_bf16 v[92:95], v[176:179], v[192:195], v[92:95]
	v_mfma_f32_16x16x32_bf16 v[84:87], v[168:171], v[224:227], v[84:87]
	v_mfma_f32_16x16x32_bf16 v[76:79], v[176:179], v[224:227], v[76:79]
	v_mfma_f32_16x16x32_bf16 v[72:75], v[168:171], v[238:241], v[72:75]
	v_mfma_f32_16x16x32_bf16 v[68:71], v[176:179], v[238:241], v[68:71]
	v_mfma_f32_16x16x32_bf16 v[116:119], v[172:175], v[188:191], v[116:119]
	v_mfma_f32_16x16x32_bf16 v[108:111], v[180:183], v[188:191], v[108:111]
	v_mfma_f32_16x16x32_bf16 v[100:103], v[172:175], v[196:199], v[100:103]
	v_mfma_f32_16x16x32_bf16 v[92:95], v[180:183], v[196:199], v[92:95]
	v_mfma_f32_16x16x32_bf16 v[84:87], v[172:175], v[228:231], v[84:87]
	v_mfma_f32_16x16x32_bf16 v[76:79], v[180:183], v[228:231], v[76:79]
	v_mfma_f32_16x16x32_bf16 v[72:75], v[172:175], v[242:245], v[72:75]
	v_mfma_f32_16x16x32_bf16 v[68:71], v[180:183], v[242:245], v[68:71]
	s_setprio 0
	s_barrier
	s_add_i32 s4, s31, s47
	v_lshl_add_u64 v[146:147], v[146:147], 0, s[78:79]
	s_mov_b32 m0, s4
	s_nop 0
	global_load_lds_dwordx4 v[146:147], off
	s_add_i32 m0, s4, 0x2000
	s_add_u32 s4, s42, 0x80080
	v_lshl_add_u64 v[146:147], v[212:213], 0, s[78:79]
	s_addc_u32 s5, s43, 0
	s_add_i32 s31, s64, s47
	global_load_lds_dwordx4 v[146:147], off
	v_lshl_add_u64 v[146:147], s[4:5], 0, v[34:35]
	s_mov_b32 m0, s31
	s_nop 0
	global_load_lds_dwordx4 v[146:147], off
	v_lshl_add_u64 v[146:147], s[4:5], 0, v[132:133]
	s_add_i32 m0, s31, 0x2000
	s_nop 0
	global_load_lds_dwordx4 v[146:147], off
	v_lshl_add_u64 v[146:147], v[232:233], 0, s[78:79]
	s_mov_b32 m0, s52
	s_nop 0
	global_load_lds_dwordx4 v[146:147], off
	v_lshl_add_u64 v[146:147], v[246:247], 0, s[78:79]
	s_mov_b32 m0, s53
	s_nop 0
	global_load_lds_dwordx4 v[146:147], off
	ds_read_b128 v[184:187], v150 offset:49152
	ds_read_b128 v[188:191], v150 offset:50176
	ds_read_b128 v[192:195], v150 offset:51200
	ds_read_b128 v[196:199], v150 offset:52224
	ds_read_b128 v[224:227], v150 offset:53248
	ds_read_b128 v[228:231], v150 offset:54272
	ds_read_b128 v[238:241], v150 offset:55296
	ds_read_b128 v[242:245], v150 offset:56320
	s_waitcnt vmcnt(8)
	s_waitcnt lgkmcnt(0)
	s_barrier
	s_setprio 1
	s_waitcnt lgkmcnt(0)
	v_mfma_f32_16x16x32_bf16 v[64:67], v[152:155], v[184:187], v[64:67]
	v_mfma_f32_16x16x32_bf16 v[60:63], v[160:163], v[184:187], v[60:63]
	v_mfma_f32_16x16x32_bf16 v[52:55], v[152:155], v[192:195], v[52:55]
	v_mfma_f32_16x16x32_bf16 v[44:47], v[160:163], v[192:195], v[44:47]
	v_mfma_f32_16x16x32_bf16 v[36:39], v[152:155], v[224:227], v[36:39]
	v_mfma_f32_16x16x32_bf16 v[26:29], v[160:163], v[224:227], v[26:29]
	v_mfma_f32_16x16x32_bf16 v[18:21], v[152:155], v[238:241], v[18:21]
	v_mfma_f32_16x16x32_bf16 v[10:13], v[160:163], v[238:241], v[10:13]
	v_mfma_f32_16x16x32_bf16 v[64:67], v[156:159], v[188:191], v[64:67]
	v_mfma_f32_16x16x32_bf16 v[60:63], v[164:167], v[188:191], v[60:63]
	v_mfma_f32_16x16x32_bf16 v[52:55], v[156:159], v[196:199], v[52:55]
	v_mfma_f32_16x16x32_bf16 v[44:47], v[164:167], v[196:199], v[44:47]
	v_mfma_f32_16x16x32_bf16 v[36:39], v[156:159], v[228:231], v[36:39]
	v_mfma_f32_16x16x32_bf16 v[26:29], v[164:167], v[228:231], v[26:29]
	v_mfma_f32_16x16x32_bf16 v[18:21], v[156:159], v[242:245], v[18:21]
	v_mfma_f32_16x16x32_bf16 v[10:13], v[164:167], v[242:245], v[10:13]
	s_setprio 0
	s_setprio 1
	v_mfma_f32_16x16x32_bf16 v[56:59], v[168:171], v[184:187], v[56:59]
	v_mfma_f32_16x16x32_bf16 v[48:51], v[176:179], v[184:187], v[48:51]
	v_mfma_f32_16x16x32_bf16 v[40:43], v[168:171], v[192:195], v[40:43]
	v_mfma_f32_16x16x32_bf16 v[30:33], v[176:179], v[192:195], v[30:33]
	v_mfma_f32_16x16x32_bf16 v[22:25], v[168:171], v[224:227], v[22:25]
	v_mfma_f32_16x16x32_bf16 v[14:17], v[176:179], v[224:227], v[14:17]
	v_mfma_f32_16x16x32_bf16 v[6:9], v[168:171], v[238:241], v[6:9]
	v_mfma_f32_16x16x32_bf16 v[2:5], v[176:179], v[238:241], v[2:5]
	v_mfma_f32_16x16x32_bf16 v[56:59], v[172:175], v[188:191], v[56:59]
	v_mfma_f32_16x16x32_bf16 v[48:51], v[180:183], v[188:191], v[48:51]
	v_mfma_f32_16x16x32_bf16 v[40:43], v[172:175], v[196:199], v[40:43]
	v_mfma_f32_16x16x32_bf16 v[30:33], v[180:183], v[196:199], v[30:33]
	v_mfma_f32_16x16x32_bf16 v[22:25], v[172:175], v[228:231], v[22:25]
	v_mfma_f32_16x16x32_bf16 v[14:17], v[180:183], v[228:231], v[14:17]
	v_mfma_f32_16x16x32_bf16 v[6:9], v[172:175], v[242:245], v[6:9]
	v_mfma_f32_16x16x32_bf16 v[2:5], v[180:183], v[242:245], v[2:5]
	s_setprio 0
	s_barrier
	s_add_i32 s29, s29, 2
	s_add_u32 s14, s14, 0x100
	s_addc_u32 s15, s15, 0
	s_add_u32 s38, s38, 0x100
	s_addc_u32 s39, s39, 0
	s_cmp_gt_u32 s29, 29
	s_cbranch_scc0 .LBB0_130
	s_and_b64 vcc, exec, s[22:23]
	s_cbranch_vccz .LBB0_133
	s_barrier

.LBB0_607:
	s_add_u32 s4, s30, 0x80
	s_addc_u32 s5, s31, 0
	s_add_i32 s53, 0, 0x10000
	s_cmp_eq_u32 s52, 28
	s_cselect_b32 s5, s27, s5
	s_cselect_b32 s4, s26, s4
	s_cselect_b32 s35, s29, s25
	s_cselect_b32 s34, s28, s23
	s_add_i32 s56, 0, 0x14000
	v_lshl_add_u64 v[198:199], s[30:31], 0, v[144:145]
	s_add_i32 m0, s42, 0xc000
	s_nop 0
	global_load_lds_dwordx4 v[198:199], off
	v_lshl_add_u64 v[198:199], s[30:31], 0, v[142:143]
	s_add_i32 m0, s42, 0xe000
	s_nop 0
	global_load_lds_dwordx4 v[198:199], off
	v_add_u32_e32 v153, s53, v150
	ds_read_b128 v[146:149], v153
	ds_read_b128 v[154:157], v153 offset:1024
	ds_read_b128 v[158:161], v153 offset:2048
	ds_read_b128 v[162:165], v153 offset:3072
	v_add_u32_e32 v153, s56, v150
	ds_read_b128 v[166:169], v153
	ds_read_b128 v[170:173], v153 offset:1024
	ds_read_b128 v[174:177], v153 offset:2048
	ds_read_b128 v[178:181], v153 offset:3072
	ds_read_b128 v[182:185], v152
	ds_read_b128 v[186:189], v152 offset:1024
	ds_read_b128 v[190:193], v152 offset:2048
	ds_read_b128 v[194:197], v152 offset:3072
	ds_read_b128 v[224:227], v152 offset:4096
	ds_read_b128 v[228:231], v152 offset:5120
	ds_read_b128 v[238:241], v152 offset:6144
	ds_read_b128 v[242:245], v152 offset:7168
	s_waitcnt vmcnt(8)
	s_waitcnt lgkmcnt(0)
	s_barrier
	s_setprio 1
	s_waitcnt lgkmcnt(0)
	v_mfma_f32_16x16x32_bf16 v[128:131], v[146:149], v[182:185], v[128:131]
	v_mfma_f32_16x16x32_bf16 v[124:127], v[158:161], v[182:185], v[124:127]
	v_mfma_f32_16x16x32_bf16 v[112:115], v[146:149], v[190:193], v[112:115]
	v_mfma_f32_16x16x32_bf16 v[108:111], v[158:161], v[190:193], v[108:111]
	v_mfma_f32_16x16x32_bf16 v[96:99], v[146:149], v[224:227], v[96:99]
	v_mfma_f32_16x16x32_bf16 v[92:95], v[158:161], v[224:227], v[92:95]
	v_mfma_f32_16x16x32_bf16 v[80:83], v[146:149], v[238:241], v[80:83]
	v_mfma_f32_16x16x32_bf16 v[76:79], v[158:161], v[238:241], v[76:79]
	v_mfma_f32_16x16x32_bf16 v[128:131], v[154:157], v[186:189], v[128:131]
	v_mfma_f32_16x16x32_bf16 v[124:127], v[162:165], v[186:189], v[124:127]
	v_mfma_f32_16x16x32_bf16 v[112:115], v[154:157], v[194:197], v[112:115]
	v_mfma_f32_16x16x32_bf16 v[108:111], v[162:165], v[194:197], v[108:111]
	v_mfma_f32_16x16x32_bf16 v[96:99], v[154:157], v[228:231], v[96:99]
	v_mfma_f32_16x16x32_bf16 v[92:95], v[162:165], v[228:231], v[92:95]
	v_mfma_f32_16x16x32_bf16 v[80:83], v[154:157], v[242:245], v[80:83]
	v_mfma_f32_16x16x32_bf16 v[76:79], v[162:165], v[242:245], v[76:79]
	s_setprio 0
	s_setprio 1
	v_mfma_f32_16x16x32_bf16 v[120:123], v[166:169], v[182:185], v[120:123]
	v_mfma_f32_16x16x32_bf16 v[116:119], v[174:177], v[182:185], v[116:119]
	v_mfma_f32_16x16x32_bf16 v[104:107], v[166:169], v[190:193], v[104:107]
	v_mfma_f32_16x16x32_bf16 v[100:103], v[174:177], v[190:193], v[100:103]
	v_mfma_f32_16x16x32_bf16 v[88:91], v[166:169], v[224:227], v[88:91]
	v_mfma_f32_16x16x32_bf16 v[84:87], v[174:177], v[224:227], v[84:87]
	v_mfma_f32_16x16x32_bf16 v[72:75], v[166:169], v[238:241], v[72:75]
	v_mfma_f32_16x16x32_bf16 v[68:71], v[174:177], v[238:241], v[68:71]
	v_mfma_f32_16x16x32_bf16 v[120:123], v[170:173], v[186:189], v[120:123]
	v_mfma_f32_16x16x32_bf16 v[116:119], v[178:181], v[186:189], v[116:119]
	v_mfma_f32_16x16x32_bf16 v[104:107], v[170:173], v[194:197], v[104:107]
	v_mfma_f32_16x16x32_bf16 v[100:103], v[178:181], v[194:197], v[100:103]
	v_mfma_f32_16x16x32_bf16 v[88:91], v[170:173], v[228:231], v[88:91]
	v_mfma_f32_16x16x32_bf16 v[84:87], v[178:181], v[228:231], v[84:87]
	v_mfma_f32_16x16x32_bf16 v[72:75], v[170:173], v[242:245], v[72:75]
	v_mfma_f32_16x16x32_bf16 v[68:71], v[178:181], v[242:245], v[68:71]
	s_setprio 0
	s_barrier
	s_add_i32 s53, s53, s39
	v_lshl_add_u64 v[198:199], s[34:35], 0, v[34:35]
	s_mov_b32 m0, s53
	s_nop 0
	global_load_lds_dwordx4 v[198:199], off
	s_add_i32 m0, s53, 0x2000
	s_add_u32 s54, s34, 0x80000
	v_lshl_add_u64 v[212:213], s[34:35], 0, v[132:133]
	s_addc_u32 s55, s35, 0
	s_add_i32 s53, s56, s39
	global_load_lds_dwordx4 v[212:213], off
	v_lshl_add_u64 v[232:233], s[54:55], 0, v[34:35]
	s_mov_b32 m0, s53
	v_lshl_add_u64 v[246:247], s[4:5], 0, v[134:135]
	global_load_lds_dwordx4 v[232:233], off
	v_lshl_add_u64 v[232:233], s[54:55], 0, v[132:133]
	s_add_i32 m0, s53, 0x2000
	s_nop 0
	global_load_lds_dwordx4 v[232:233], off
	v_lshl_add_u64 v[232:233], s[4:5], 0, v[138:139]
	s_mov_b32 m0, s42
	s_nop 0
	global_load_lds_dwordx4 v[232:233], off
	s_mov_b32 m0, s43
	s_nop 0
	global_load_lds_dwordx4 v[246:247], off
	ds_read_b128 v[182:185], v152 offset:16384
	ds_read_b128 v[186:189], v152 offset:17408
	ds_read_b128 v[190:193], v152 offset:18432
	ds_read_b128 v[194:197], v152 offset:19456
	ds_read_b128 v[224:227], v152 offset:20480
	ds_read_b128 v[228:231], v152 offset:21504
	ds_read_b128 v[238:241], v152 offset:22528
	ds_read_b128 v[242:245], v152 offset:23552
	s_waitcnt vmcnt(8)
	s_waitcnt lgkmcnt(0)
	s_barrier
	s_setprio 1
	s_waitcnt lgkmcnt(0)
	v_mfma_f32_16x16x32_bf16 v[64:67], v[146:149], v[182:185], v[64:67]
	v_mfma_f32_16x16x32_bf16 v[60:63], v[158:161], v[182:185], v[60:63]
	v_mfma_f32_16x16x32_bf16 v[48:51], v[146:149], v[190:193], v[48:51]
	v_mfma_f32_16x16x32_bf16 v[44:47], v[158:161], v[190:193], v[44:47]
	v_mfma_f32_16x16x32_bf16 v[30:33], v[146:149], v[224:227], v[30:33]
	v_mfma_f32_16x16x32_bf16 v[26:29], v[158:161], v[224:227], v[26:29]
	v_mfma_f32_16x16x32_bf16 v[14:17], v[146:149], v[238:241], v[14:17]
	v_mfma_f32_16x16x32_bf16 v[10:13], v[158:161], v[238:241], v[10:13]
	v_mfma_f32_16x16x32_bf16 v[64:67], v[154:157], v[186:189], v[64:67]
	v_mfma_f32_16x16x32_bf16 v[60:63], v[162:165], v[186:189], v[60:63]
	v_mfma_f32_16x16x32_bf16 v[48:51], v[154:157], v[194:197], v[48:51]
	v_mfma_f32_16x16x32_bf16 v[44:47], v[162:165], v[194:197], v[44:47]
	v_mfma_f32_16x16x32_bf16 v[30:33], v[154:157], v[228:231], v[30:33]
	v_mfma_f32_16x16x32_bf16 v[26:29], v[162:165], v[228:231], v[26:29]
	v_mfma_f32_16x16x32_bf16 v[14:17], v[154:157], v[242:245], v[14:17]
	v_mfma_f32_16x16x32_bf16 v[10:13], v[162:165], v[242:245], v[10:13]
	s_setprio 0
	s_setprio 1
	v_mfma_f32_16x16x32_bf16 v[56:59], v[166:169], v[182:185], v[56:59]
	v_mfma_f32_16x16x32_bf16 v[52:55], v[174:177], v[182:185], v[52:55]
	v_mfma_f32_16x16x32_bf16 v[40:43], v[166:169], v[190:193], v[40:43]
	v_mfma_f32_16x16x32_bf16 v[36:39], v[174:177], v[190:193], v[36:39]
	v_mfma_f32_16x16x32_bf16 v[22:25], v[166:169], v[224:227], v[22:25]
	v_mfma_f32_16x16x32_bf16 v[18:21], v[174:177], v[224:227], v[18:21]
	v_mfma_f32_16x16x32_bf16 v[6:9], v[166:169], v[238:241], v[6:9]
	v_mfma_f32_16x16x32_bf16 v[2:5], v[174:177], v[238:241], v[2:5]
	v_mfma_f32_16x16x32_bf16 v[56:59], v[170:173], v[186:189], v[56:59]
	v_mfma_f32_16x16x32_bf16 v[52:55], v[178:181], v[186:189], v[52:55]
	v_mfma_f32_16x16x32_bf16 v[40:43], v[170:173], v[194:197], v[40:43]
	v_mfma_f32_16x16x32_bf16 v[36:39], v[178:181], v[194:197], v[36:39]
	v_mfma_f32_16x16x32_bf16 v[22:25], v[170:173], v[228:231], v[22:25]
	v_mfma_f32_16x16x32_bf16 v[18:21], v[178:181], v[228:231], v[18:21]
	v_mfma_f32_16x16x32_bf16 v[6:9], v[170:173], v[242:245], v[6:9]
	v_mfma_f32_16x16x32_bf16 v[2:5], v[178:181], v[242:245], v[2:5]
	s_setprio 0
	s_barrier
	s_add_i32 s53, 0, 0x18000
	s_add_i32 s54, 0, 0x1c000
	s_mov_b32 m0, s44
	v_lshl_add_u64 v[248:249], s[4:5], 0, v[140:141]
	global_load_lds_dwordx4 v[248:249], off
	v_lshl_add_u64 v[248:249], s[4:5], 0, v[136:137]
	s_mov_b32 m0, s45
	s_nop 0
	global_load_lds_dwordx4 v[248:249], off
	v_add_u32_e32 v153, s53, v150
	ds_read_b128 v[146:149], v153
	ds_read_b128 v[154:157], v153 offset:1024
	ds_read_b128 v[158:161], v153 offset:2048
	ds_read_b128 v[162:165], v153 offset:3072
	v_add_u32_e32 v153, s54, v150
	ds_read_b128 v[166:169], v153
	ds_read_b128 v[170:173], v153 offset:1024
	ds_read_b128 v[174:177], v153 offset:2048
	ds_read_b128 v[178:181], v153 offset:3072
	ds_read_b128 v[182:185], v152 offset:32768
	ds_read_b128 v[186:189], v152 offset:33792
	ds_read_b128 v[190:193], v152 offset:34816
	ds_read_b128 v[194:197], v152 offset:35840
	ds_read_b128 v[224:227], v152 offset:36864
	ds_read_b128 v[228:231], v152 offset:37888
	ds_read_b128 v[238:241], v152 offset:38912
	ds_read_b128 v[242:245], v152 offset:39936
	s_waitcnt vmcnt(8)
	s_waitcnt lgkmcnt(0)
	s_barrier
	s_setprio 1
	s_waitcnt lgkmcnt(0)
	v_mfma_f32_16x16x32_bf16 v[128:131], v[146:149], v[182:185], v[128:131]
	v_mfma_f32_16x16x32_bf16 v[124:127], v[158:161], v[182:185], v[124:127]
	v_mfma_f32_16x16x32_bf16 v[112:115], v[146:149], v[190:193], v[112:115]
	v_mfma_f32_16x16x32_bf16 v[108:111], v[158:161], v[190:193], v[108:111]
	v_mfma_f32_16x16x32_bf16 v[96:99], v[146:149], v[224:227], v[96:99]
	v_mfma_f32_16x16x32_bf16 v[92:95], v[158:161], v[224:227], v[92:95]
	v_mfma_f32_16x16x32_bf16 v[80:83], v[146:149], v[238:241], v[80:83]
	v_mfma_f32_16x16x32_bf16 v[76:79], v[158:161], v[238:241], v[76:79]
	v_mfma_f32_16x16x32_bf16 v[128:131], v[154:157], v[186:189], v[128:131]
	v_mfma_f32_16x16x32_bf16 v[124:127], v[162:165], v[186:189], v[124:127]
	v_mfma_f32_16x16x32_bf16 v[112:115], v[154:157], v[194:197], v[112:115]
	v_mfma_f32_16x16x32_bf16 v[108:111], v[162:165], v[194:197], v[108:111]
	v_mfma_f32_16x16x32_bf16 v[96:99], v[154:157], v[228:231], v[96:99]
	v_mfma_f32_16x16x32_bf16 v[92:95], v[162:165], v[228:231], v[92:95]
	v_mfma_f32_16x16x32_bf16 v[80:83], v[154:157], v[242:245], v[80:83]
	v_mfma_f32_16x16x32_bf16 v[76:79], v[162:165], v[242:245], v[76:79]
	s_setprio 0
	s_setprio 1
	v_mfma_f32_16x16x32_bf16 v[120:123], v[166:169], v[182:185], v[120:123]
	v_mfma_f32_16x16x32_bf16 v[116:119], v[174:177], v[182:185], v[116:119]
	v_mfma_f32_16x16x32_bf16 v[104:107], v[166:169], v[190:193], v[104:107]
	v_mfma_f32_16x16x32_bf16 v[100:103], v[174:177], v[190:193], v[100:103]
	v_mfma_f32_16x16x32_bf16 v[88:91], v[166:169], v[224:227], v[88:91]
	v_mfma_f32_16x16x32_bf16 v[84:87], v[174:177], v[224:227], v[84:87]
	v_mfma_f32_16x16x32_bf16 v[72:75], v[166:169], v[238:241], v[72:75]
	v_mfma_f32_16x16x32_bf16 v[68:71], v[174:177], v[238:241], v[68:71]
	v_mfma_f32_16x16x32_bf16 v[120:123], v[170:173], v[186:189], v[120:123]
	v_mfma_f32_16x16x32_bf16 v[116:119], v[178:181], v[186:189], v[116:119]
	v_mfma_f32_16x16x32_bf16 v[104:107], v[170:173], v[194:197], v[104:107]
	v_mfma_f32_16x16x32_bf16 v[100:103], v[178:181], v[194:197], v[100:103]
	v_mfma_f32_16x16x32_bf16 v[88:91], v[170:173], v[228:231], v[88:91]
	v_mfma_f32_16x16x32_bf16 v[84:87], v[178:181], v[228:231], v[84:87]
	v_mfma_f32_16x16x32_bf16 v[72:75], v[170:173], v[242:245], v[72:75]
	v_mfma_f32_16x16x32_bf16 v[68:71], v[178:181], v[242:245], v[68:71]
	s_setprio 0
	s_barrier
	s_add_i32 s4, s53, s39
	v_lshl_add_u64 v[198:199], v[198:199], 0, s[78:79]
	s_mov_b32 m0, s4
	s_nop 0
	global_load_lds_dwordx4 v[198:199], off
	s_add_i32 m0, s4, 0x2000
	s_add_u32 s4, s34, 0x80080
	v_lshl_add_u64 v[198:199], v[212:213], 0, s[78:79]
	s_addc_u32 s5, s35, 0
	s_add_i32 s34, s54, s39
	global_load_lds_dwordx4 v[198:199], off
	v_lshl_add_u64 v[198:199], s[4:5], 0, v[34:35]
	s_mov_b32 m0, s34
	s_nop 0
	global_load_lds_dwordx4 v[198:199], off
	v_lshl_add_u64 v[198:199], s[4:5], 0, v[132:133]
	s_add_i32 m0, s34, 0x2000
	s_nop 0
	global_load_lds_dwordx4 v[198:199], off
	v_lshl_add_u64 v[198:199], v[232:233], 0, s[78:79]
	s_mov_b32 m0, s46
	s_nop 0
	global_load_lds_dwordx4 v[198:199], off
	v_lshl_add_u64 v[198:199], v[246:247], 0, s[78:79]
	s_mov_b32 m0, s47
	s_nop 0
	global_load_lds_dwordx4 v[198:199], off
	ds_read_b128 v[182:185], v152 offset:49152
	ds_read_b128 v[186:189], v152 offset:50176
	ds_read_b128 v[190:193], v152 offset:51200
	ds_read_b128 v[194:197], v152 offset:52224
	ds_read_b128 v[224:227], v152 offset:53248
	ds_read_b128 v[228:231], v152 offset:54272
	ds_read_b128 v[238:241], v152 offset:55296
	ds_read_b128 v[242:245], v152 offset:56320
	s_waitcnt vmcnt(8)
	s_waitcnt lgkmcnt(0)
	s_barrier
	s_setprio 1
	s_waitcnt lgkmcnt(0)
	v_mfma_f32_16x16x32_bf16 v[64:67], v[146:149], v[182:185], v[64:67]
	v_mfma_f32_16x16x32_bf16 v[60:63], v[158:161], v[182:185], v[60:63]
	v_mfma_f32_16x16x32_bf16 v[48:51], v[146:149], v[190:193], v[48:51]
	v_mfma_f32_16x16x32_bf16 v[44:47], v[158:161], v[190:193], v[44:47]
	v_mfma_f32_16x16x32_bf16 v[30:33], v[146:149], v[224:227], v[30:33]
	v_mfma_f32_16x16x32_bf16 v[26:29], v[158:161], v[224:227], v[26:29]
	v_mfma_f32_16x16x32_bf16 v[14:17], v[146:149], v[238:241], v[14:17]
	v_mfma_f32_16x16x32_bf16 v[10:13], v[158:161], v[238:241], v[10:13]
	v_mfma_f32_16x16x32_bf16 v[64:67], v[154:157], v[186:189], v[64:67]
	v_mfma_f32_16x16x32_bf16 v[60:63], v[162:165], v[186:189], v[60:63]
	v_mfma_f32_16x16x32_bf16 v[48:51], v[154:157], v[194:197], v[48:51]
	v_mfma_f32_16x16x32_bf16 v[44:47], v[162:165], v[194:197], v[44:47]
	v_mfma_f32_16x16x32_bf16 v[30:33], v[154:157], v[228:231], v[30:33]
	v_mfma_f32_16x16x32_bf16 v[26:29], v[162:165], v[228:231], v[26:29]
	v_mfma_f32_16x16x32_bf16 v[14:17], v[154:157], v[242:245], v[14:17]
	v_mfma_f32_16x16x32_bf16 v[10:13], v[162:165], v[242:245], v[10:13]
	s_setprio 0
	s_setprio 1
	v_mfma_f32_16x16x32_bf16 v[56:59], v[166:169], v[182:185], v[56:59]
	v_mfma_f32_16x16x32_bf16 v[52:55], v[174:177], v[182:185], v[52:55]
	v_mfma_f32_16x16x32_bf16 v[40:43], v[166:169], v[190:193], v[40:43]
	v_mfma_f32_16x16x32_bf16 v[36:39], v[174:177], v[190:193], v[36:39]
	v_mfma_f32_16x16x32_bf16 v[22:25], v[166:169], v[224:227], v[22:25]
	v_mfma_f32_16x16x32_bf16 v[18:21], v[174:177], v[224:227], v[18:21]
	v_mfma_f32_16x16x32_bf16 v[6:9], v[166:169], v[238:241], v[6:9]
	v_mfma_f32_16x16x32_bf16 v[2:5], v[174:177], v[238:241], v[2:5]
	v_mfma_f32_16x16x32_bf16 v[56:59], v[170:173], v[186:189], v[56:59]
	v_mfma_f32_16x16x32_bf16 v[52:55], v[178:181], v[186:189], v[52:55]
	v_mfma_f32_16x16x32_bf16 v[40:43], v[170:173], v[194:197], v[40:43]
	v_mfma_f32_16x16x32_bf16 v[36:39], v[178:181], v[194:197], v[36:39]
	v_mfma_f32_16x16x32_bf16 v[22:25], v[170:173], v[228:231], v[22:25]
	v_mfma_f32_16x16x32_bf16 v[18:21], v[178:181], v[228:231], v[18:21]
	v_mfma_f32_16x16x32_bf16 v[6:9], v[170:173], v[242:245], v[6:9]
	v_mfma_f32_16x16x32_bf16 v[2:5], v[178:181], v[242:245], v[2:5]
	s_setprio 0
	s_barrier
	s_add_i32 s52, s52, 2
	s_add_u32 s23, s23, 0x100
	s_addc_u32 s25, s25, 0
	s_add_u32 s30, s30, 0x100
	s_addc_u32 s31, s31, 0
	s_cmp_gt_u32 s52, 29
	s_cbranch_scc0 .LBB0_607
	s_and_b64 vcc, exec, s[20:21]
	s_cbranch_vccz .LBB0_610
	s_barrier

.LBB0_673:
	s_add_u32 s4, s30, 0x80
	s_addc_u32 s5, s31, 0
	s_add_i32 s64, 0, 0x10000
	s_cmp_eq_u32 s57, 12
	s_cselect_b32 s5, s27, s5
	s_cselect_b32 s4, s26, s4
	s_cselect_b32 s35, s29, s25
	s_cselect_b32 s34, s28, s23
	s_add_i32 s68, 0, 0x14000
	v_lshl_add_u64 v[164:165], s[30:31], 0, v[178:179]
	s_add_i32 m0, s38, 0xc000
	s_nop 0
	global_load_lds_dwordx4 v[164:165], off
	v_lshl_add_u64 v[164:165], s[30:31], 0, v[176:177]
	s_add_i32 m0, s38, 0xe000
	s_nop 0
	global_load_lds_dwordx4 v[164:165], off
	v_add_u32_e32 v144, s64, v190
	v_add_u32_e32 v160, s68, v190
	ds_read_b128 v[132:135], v144
	ds_read_b128 v[136:139], v144 offset:1024
	ds_read_b128 v[140:143], v144 offset:2048
	ds_read_b128 v[144:147], v144 offset:3072
	ds_read_b128 v[148:151], v160
	ds_read_b128 v[152:155], v160 offset:1024
	ds_read_b128 v[156:159], v160 offset:2048
	ds_read_b128 v[160:163], v160 offset:3072
	ds_read_b128 v[180:183], v192
	ds_read_b128 v[184:187], v192 offset:1024
	ds_read_b128 v[194:197], v192 offset:2048
	ds_read_b128 v[224:227], v192 offset:3072
	ds_read_b128 v[228:231], v192 offset:4096
	ds_read_b128 v[238:241], v192 offset:5120
	ds_read_b128 v[242:245], v192 offset:6144
	ds_read_b128 v[246:249], v192 offset:7168
	s_waitcnt vmcnt(8)
	s_waitcnt lgkmcnt(0)
	s_barrier
	s_setprio 1
	s_waitcnt lgkmcnt(0)
	v_mfma_f32_16x16x32_bf16 v[128:131], v[132:135], v[180:183], v[128:131]
	v_mfma_f32_16x16x32_bf16 v[124:127], v[140:143], v[180:183], v[124:127]
	v_mfma_f32_16x16x32_bf16 v[112:115], v[132:135], v[194:197], v[112:115]
	v_mfma_f32_16x16x32_bf16 v[108:111], v[140:143], v[194:197], v[108:111]
	v_mfma_f32_16x16x32_bf16 v[96:99], v[132:135], v[228:231], v[96:99]
	v_mfma_f32_16x16x32_bf16 v[92:95], v[140:143], v[228:231], v[92:95]
	v_mfma_f32_16x16x32_bf16 v[80:83], v[132:135], v[242:245], v[80:83]
	v_mfma_f32_16x16x32_bf16 v[76:79], v[140:143], v[242:245], v[76:79]
	v_mfma_f32_16x16x32_bf16 v[128:131], v[136:139], v[184:187], v[128:131]
	v_mfma_f32_16x16x32_bf16 v[124:127], v[144:147], v[184:187], v[124:127]
	v_mfma_f32_16x16x32_bf16 v[112:115], v[136:139], v[224:227], v[112:115]
	v_mfma_f32_16x16x32_bf16 v[108:111], v[144:147], v[224:227], v[108:111]
	v_mfma_f32_16x16x32_bf16 v[96:99], v[136:139], v[238:241], v[96:99]
	v_mfma_f32_16x16x32_bf16 v[92:95], v[144:147], v[238:241], v[92:95]
	v_mfma_f32_16x16x32_bf16 v[80:83], v[136:139], v[246:249], v[80:83]
	v_mfma_f32_16x16x32_bf16 v[76:79], v[144:147], v[246:249], v[76:79]
	s_setprio 0
	s_setprio 1
	v_mfma_f32_16x16x32_bf16 v[120:123], v[148:151], v[180:183], v[120:123]
	v_mfma_f32_16x16x32_bf16 v[116:119], v[156:159], v[180:183], v[116:119]
	v_mfma_f32_16x16x32_bf16 v[104:107], v[148:151], v[194:197], v[104:107]
	v_mfma_f32_16x16x32_bf16 v[100:103], v[156:159], v[194:197], v[100:103]
	v_mfma_f32_16x16x32_bf16 v[88:91], v[148:151], v[228:231], v[88:91]
	v_mfma_f32_16x16x32_bf16 v[84:87], v[156:159], v[228:231], v[84:87]
	v_mfma_f32_16x16x32_bf16 v[72:75], v[148:151], v[242:245], v[72:75]
	v_mfma_f32_16x16x32_bf16 v[68:71], v[156:159], v[242:245], v[68:71]
	v_mfma_f32_16x16x32_bf16 v[120:123], v[152:155], v[184:187], v[120:123]
	v_mfma_f32_16x16x32_bf16 v[116:119], v[160:163], v[184:187], v[116:119]
	v_mfma_f32_16x16x32_bf16 v[104:107], v[152:155], v[224:227], v[104:107]
	v_mfma_f32_16x16x32_bf16 v[100:103], v[160:163], v[224:227], v[100:103]
	v_mfma_f32_16x16x32_bf16 v[88:91], v[152:155], v[238:241], v[88:91]
	v_mfma_f32_16x16x32_bf16 v[84:87], v[160:163], v[238:241], v[84:87]
	v_mfma_f32_16x16x32_bf16 v[72:75], v[152:155], v[246:249], v[72:75]
	v_mfma_f32_16x16x32_bf16 v[68:71], v[160:163], v[246:249], v[68:71]
	s_setprio 0
	s_barrier
	s_add_i32 s64, s64, s37
	v_lshl_add_u64 v[164:165], s[34:35], 0, v[34:35]
	s_mov_b32 m0, s64
	s_nop 0
	global_load_lds_dwordx4 v[164:165], off
	s_add_i32 m0, s64, 0x2000
	s_add_u32 s64, s34, 0x40000
	v_lshl_add_u64 v[188:189], s[34:35], 0, v[174:175]
	s_addc_u32 s65, s35, 0
	s_add_i32 s68, s68, s37
	global_load_lds_dwordx4 v[188:189], off
	v_lshl_add_u64 v[198:199], s[64:65], 0, v[34:35]
	s_mov_b32 m0, s68
	v_lshl_add_u64 v[212:213], s[4:5], 0, v[170:171]
	global_load_lds_dwordx4 v[198:199], off
	v_lshl_add_u64 v[198:199], s[64:65], 0, v[174:175]
	s_add_i32 m0, s68, 0x2000
	s_nop 0
	global_load_lds_dwordx4 v[198:199], off
	v_lshl_add_u64 v[198:199], s[4:5], 0, v[166:167]
	s_mov_b32 m0, s38
	s_nop 0
	global_load_lds_dwordx4 v[198:199], off
	s_mov_b32 m0, s39
	s_nop 0
	global_load_lds_dwordx4 v[212:213], off
	ds_read_b128 v[180:183], v192 offset:16384
	ds_read_b128 v[184:187], v192 offset:17408
	ds_read_b128 v[194:197], v192 offset:18432
	ds_read_b128 v[224:227], v192 offset:19456
	ds_read_b128 v[228:231], v192 offset:20480
	ds_read_b128 v[238:241], v192 offset:21504
	ds_read_b128 v[242:245], v192 offset:22528
	ds_read_b128 v[246:249], v192 offset:23552
	s_waitcnt vmcnt(8)
	s_waitcnt lgkmcnt(0)
	s_barrier
	s_setprio 1
	s_waitcnt lgkmcnt(0)
	v_mfma_f32_16x16x32_bf16 v[64:67], v[132:135], v[180:183], v[64:67]
	v_mfma_f32_16x16x32_bf16 v[60:63], v[140:143], v[180:183], v[60:63]
	v_mfma_f32_16x16x32_bf16 v[48:51], v[132:135], v[194:197], v[48:51]
	v_mfma_f32_16x16x32_bf16 v[44:47], v[140:143], v[194:197], v[44:47]
	v_mfma_f32_16x16x32_bf16 v[30:33], v[132:135], v[228:231], v[30:33]
	v_mfma_f32_16x16x32_bf16 v[26:29], v[140:143], v[228:231], v[26:29]
	v_mfma_f32_16x16x32_bf16 v[14:17], v[132:135], v[242:245], v[14:17]
	v_mfma_f32_16x16x32_bf16 v[10:13], v[140:143], v[242:245], v[10:13]
	v_mfma_f32_16x16x32_bf16 v[64:67], v[136:139], v[184:187], v[64:67]
	v_mfma_f32_16x16x32_bf16 v[60:63], v[144:147], v[184:187], v[60:63]
	v_mfma_f32_16x16x32_bf16 v[48:51], v[136:139], v[224:227], v[48:51]
	v_mfma_f32_16x16x32_bf16 v[44:47], v[144:147], v[224:227], v[44:47]
	v_mfma_f32_16x16x32_bf16 v[30:33], v[136:139], v[238:241], v[30:33]
	v_mfma_f32_16x16x32_bf16 v[26:29], v[144:147], v[238:241], v[26:29]
	v_mfma_f32_16x16x32_bf16 v[14:17], v[136:139], v[246:249], v[14:17]
	v_mfma_f32_16x16x32_bf16 v[10:13], v[144:147], v[246:249], v[10:13]
	s_setprio 0
	s_setprio 1
	v_mfma_f32_16x16x32_bf16 v[56:59], v[148:151], v[180:183], v[56:59]
	v_mfma_f32_16x16x32_bf16 v[52:55], v[156:159], v[180:183], v[52:55]
	v_mfma_f32_16x16x32_bf16 v[40:43], v[148:151], v[194:197], v[40:43]
	v_mfma_f32_16x16x32_bf16 v[36:39], v[156:159], v[194:197], v[36:39]
	v_mfma_f32_16x16x32_bf16 v[22:25], v[148:151], v[228:231], v[22:25]
	v_mfma_f32_16x16x32_bf16 v[18:21], v[156:159], v[228:231], v[18:21]
	v_mfma_f32_16x16x32_bf16 v[6:9], v[148:151], v[242:245], v[6:9]
	v_mfma_f32_16x16x32_bf16 v[2:5], v[156:159], v[242:245], v[2:5]
	v_mfma_f32_16x16x32_bf16 v[56:59], v[152:155], v[184:187], v[56:59]
	v_mfma_f32_16x16x32_bf16 v[52:55], v[160:163], v[184:187], v[52:55]
	v_mfma_f32_16x16x32_bf16 v[40:43], v[152:155], v[224:227], v[40:43]
	v_mfma_f32_16x16x32_bf16 v[36:39], v[160:163], v[224:227], v[36:39]
	v_mfma_f32_16x16x32_bf16 v[22:25], v[152:155], v[238:241], v[22:25]
	v_mfma_f32_16x16x32_bf16 v[18:21], v[160:163], v[238:241], v[18:21]
	v_mfma_f32_16x16x32_bf16 v[6:9], v[152:155], v[246:249], v[6:9]
	v_mfma_f32_16x16x32_bf16 v[2:5], v[160:163], v[246:249], v[2:5]
	s_setprio 0
	s_barrier
	s_add_i32 s64, 0, 0x18000
	s_add_i32 s65, 0, 0x1c000
	s_mov_b32 m0, s46
	v_lshl_add_u64 v[232:233], s[4:5], 0, v[168:169]
	global_load_lds_dwordx4 v[232:233], off
	v_lshl_add_u64 v[232:233], s[4:5], 0, v[172:173]
	s_mov_b32 m0, s47
	s_nop 0
	global_load_lds_dwordx4 v[232:233], off
	v_add_u32_e32 v144, s64, v190
	v_add_u32_e32 v160, s65, v190
	ds_read_b128 v[132:135], v144
	ds_read_b128 v[136:139], v144 offset:1024
	ds_read_b128 v[140:143], v144 offset:2048
	ds_read_b128 v[144:147], v144 offset:3072
	ds_read_b128 v[148:151], v160
	ds_read_b128 v[152:155], v160 offset:1024
	ds_read_b128 v[156:159], v160 offset:2048
	ds_read_b128 v[160:163], v160 offset:3072
	ds_read_b128 v[180:183], v192 offset:32768
	ds_read_b128 v[184:187], v192 offset:33792
	ds_read_b128 v[194:197], v192 offset:34816
	ds_read_b128 v[224:227], v192 offset:35840
	ds_read_b128 v[228:231], v192 offset:36864
	ds_read_b128 v[238:241], v192 offset:37888
	ds_read_b128 v[242:245], v192 offset:38912
	ds_read_b128 v[246:249], v192 offset:39936
	s_waitcnt vmcnt(8)
	s_waitcnt lgkmcnt(0)
	s_barrier
	s_setprio 1
	s_waitcnt lgkmcnt(0)
	v_mfma_f32_16x16x32_bf16 v[128:131], v[132:135], v[180:183], v[128:131]
	v_mfma_f32_16x16x32_bf16 v[124:127], v[140:143], v[180:183], v[124:127]
	v_mfma_f32_16x16x32_bf16 v[112:115], v[132:135], v[194:197], v[112:115]
	v_mfma_f32_16x16x32_bf16 v[108:111], v[140:143], v[194:197], v[108:111]
	v_mfma_f32_16x16x32_bf16 v[96:99], v[132:135], v[228:231], v[96:99]
	v_mfma_f32_16x16x32_bf16 v[92:95], v[140:143], v[228:231], v[92:95]
	v_mfma_f32_16x16x32_bf16 v[80:83], v[132:135], v[242:245], v[80:83]
	v_mfma_f32_16x16x32_bf16 v[76:79], v[140:143], v[242:245], v[76:79]
	v_mfma_f32_16x16x32_bf16 v[128:131], v[136:139], v[184:187], v[128:131]
	v_mfma_f32_16x16x32_bf16 v[124:127], v[144:147], v[184:187], v[124:127]
	v_mfma_f32_16x16x32_bf16 v[112:115], v[136:139], v[224:227], v[112:115]
	v_mfma_f32_16x16x32_bf16 v[108:111], v[144:147], v[224:227], v[108:111]
	v_mfma_f32_16x16x32_bf16 v[96:99], v[136:139], v[238:241], v[96:99]
	v_mfma_f32_16x16x32_bf16 v[92:95], v[144:147], v[238:241], v[92:95]
	v_mfma_f32_16x16x32_bf16 v[80:83], v[136:139], v[246:249], v[80:83]
	v_mfma_f32_16x16x32_bf16 v[76:79], v[144:147], v[246:249], v[76:79]
	s_setprio 0
	s_setprio 1
	v_mfma_f32_16x16x32_bf16 v[120:123], v[148:151], v[180:183], v[120:123]
	v_mfma_f32_16x16x32_bf16 v[116:119], v[156:159], v[180:183], v[116:119]
	v_mfma_f32_16x16x32_bf16 v[104:107], v[148:151], v[194:197], v[104:107]
	v_mfma_f32_16x16x32_bf16 v[100:103], v[156:159], v[194:197], v[100:103]
	v_mfma_f32_16x16x32_bf16 v[88:91], v[148:151], v[228:231], v[88:91]
	v_mfma_f32_16x16x32_bf16 v[84:87], v[156:159], v[228:231], v[84:87]
	v_mfma_f32_16x16x32_bf16 v[72:75], v[148:151], v[242:245], v[72:75]
	v_mfma_f32_16x16x32_bf16 v[68:71], v[156:159], v[242:245], v[68:71]
	v_mfma_f32_16x16x32_bf16 v[120:123], v[152:155], v[184:187], v[120:123]
	v_mfma_f32_16x16x32_bf16 v[116:119], v[160:163], v[184:187], v[116:119]
	v_mfma_f32_16x16x32_bf16 v[104:107], v[152:155], v[224:227], v[104:107]
	v_mfma_f32_16x16x32_bf16 v[100:103], v[160:163], v[224:227], v[100:103]
	v_mfma_f32_16x16x32_bf16 v[88:91], v[152:155], v[238:241], v[88:91]
	v_mfma_f32_16x16x32_bf16 v[84:87], v[160:163], v[238:241], v[84:87]
	v_mfma_f32_16x16x32_bf16 v[72:75], v[152:155], v[246:249], v[72:75]
	v_mfma_f32_16x16x32_bf16 v[68:71], v[160:163], v[246:249], v[68:71]
	s_setprio 0
	s_barrier
	s_add_i32 s4, s64, s37
	v_lshl_add_u64 v[164:165], v[164:165], 0, s[78:79]
	s_mov_b32 m0, s4
	s_nop 0
	global_load_lds_dwordx4 v[164:165], off
	s_add_i32 m0, s4, 0x2000
	s_add_u32 s4, s34, 0x40080
	v_lshl_add_u64 v[164:165], v[188:189], 0, s[78:79]
	s_addc_u32 s5, s35, 0
	s_add_i32 s34, s65, s37
	global_load_lds_dwordx4 v[164:165], off
	v_lshl_add_u64 v[164:165], s[4:5], 0, v[34:35]
	s_mov_b32 m0, s34
	s_nop 0
	global_load_lds_dwordx4 v[164:165], off
	v_lshl_add_u64 v[164:165], s[4:5], 0, v[174:175]
	s_add_i32 m0, s34, 0x2000
	s_nop 0
	global_load_lds_dwordx4 v[164:165], off
	v_lshl_add_u64 v[164:165], v[198:199], 0, s[78:79]
	s_mov_b32 m0, s52
	s_nop 0
	global_load_lds_dwordx4 v[164:165], off
	v_lshl_add_u64 v[164:165], v[212:213], 0, s[78:79]
	s_mov_b32 m0, s53
	s_nop 0
	global_load_lds_dwordx4 v[164:165], off
	ds_read_b128 v[180:183], v192 offset:49152
	ds_read_b128 v[184:187], v192 offset:50176
	ds_read_b128 v[194:197], v192 offset:51200
	ds_read_b128 v[224:227], v192 offset:52224
	ds_read_b128 v[228:231], v192 offset:53248
	ds_read_b128 v[238:241], v192 offset:54272
	ds_read_b128 v[242:245], v192 offset:55296
	ds_read_b128 v[246:249], v192 offset:56320
	s_waitcnt vmcnt(8)
	s_waitcnt lgkmcnt(0)
	s_barrier
	s_setprio 1
	s_waitcnt lgkmcnt(0)
	v_mfma_f32_16x16x32_bf16 v[64:67], v[132:135], v[180:183], v[64:67]
	v_mfma_f32_16x16x32_bf16 v[60:63], v[140:143], v[180:183], v[60:63]
	v_mfma_f32_16x16x32_bf16 v[48:51], v[132:135], v[194:197], v[48:51]
	v_mfma_f32_16x16x32_bf16 v[44:47], v[140:143], v[194:197], v[44:47]
	v_mfma_f32_16x16x32_bf16 v[30:33], v[132:135], v[228:231], v[30:33]
	v_mfma_f32_16x16x32_bf16 v[26:29], v[140:143], v[228:231], v[26:29]
	v_mfma_f32_16x16x32_bf16 v[14:17], v[132:135], v[242:245], v[14:17]
	v_mfma_f32_16x16x32_bf16 v[10:13], v[140:143], v[242:245], v[10:13]
	v_mfma_f32_16x16x32_bf16 v[64:67], v[136:139], v[184:187], v[64:67]
	v_mfma_f32_16x16x32_bf16 v[60:63], v[144:147], v[184:187], v[60:63]
	v_mfma_f32_16x16x32_bf16 v[48:51], v[136:139], v[224:227], v[48:51]
	v_mfma_f32_16x16x32_bf16 v[44:47], v[144:147], v[224:227], v[44:47]
	v_mfma_f32_16x16x32_bf16 v[30:33], v[136:139], v[238:241], v[30:33]
	v_mfma_f32_16x16x32_bf16 v[26:29], v[144:147], v[238:241], v[26:29]
	v_mfma_f32_16x16x32_bf16 v[14:17], v[136:139], v[246:249], v[14:17]
	v_mfma_f32_16x16x32_bf16 v[10:13], v[144:147], v[246:249], v[10:13]
	s_setprio 0
	s_setprio 1
	v_mfma_f32_16x16x32_bf16 v[56:59], v[148:151], v[180:183], v[56:59]
	v_mfma_f32_16x16x32_bf16 v[52:55], v[156:159], v[180:183], v[52:55]
	v_mfma_f32_16x16x32_bf16 v[40:43], v[148:151], v[194:197], v[40:43]
	v_mfma_f32_16x16x32_bf16 v[36:39], v[156:159], v[194:197], v[36:39]
	v_mfma_f32_16x16x32_bf16 v[22:25], v[148:151], v[228:231], v[22:25]
	v_mfma_f32_16x16x32_bf16 v[18:21], v[156:159], v[228:231], v[18:21]
	v_mfma_f32_16x16x32_bf16 v[6:9], v[148:151], v[242:245], v[6:9]
	v_mfma_f32_16x16x32_bf16 v[2:5], v[156:159], v[242:245], v[2:5]
	v_mfma_f32_16x16x32_bf16 v[56:59], v[152:155], v[184:187], v[56:59]
	v_mfma_f32_16x16x32_bf16 v[52:55], v[160:163], v[184:187], v[52:55]
	v_mfma_f32_16x16x32_bf16 v[40:43], v[152:155], v[224:227], v[40:43]
	v_mfma_f32_16x16x32_bf16 v[36:39], v[160:163], v[224:227], v[36:39]
	v_mfma_f32_16x16x32_bf16 v[22:25], v[152:155], v[238:241], v[22:25]
	v_mfma_f32_16x16x32_bf16 v[18:21], v[160:163], v[238:241], v[18:21]
	v_mfma_f32_16x16x32_bf16 v[6:9], v[152:155], v[246:249], v[6:9]
	v_mfma_f32_16x16x32_bf16 v[2:5], v[160:163], v[246:249], v[2:5]
	s_setprio 0
	s_barrier
	s_add_i32 s57, s57, 2
	s_add_u32 s23, s23, 0x100
	s_addc_u32 s25, s25, 0
	s_add_u32 s30, s30, 0x100
	s_addc_u32 s31, s31, 0
	s_cmp_gt_u32 s57, 13
	s_cbranch_scc0 .LBB0_673
	s_and_b64 vcc, exec, s[20:21]
	s_cbranch_vccz .LBB0_676
	s_barrier

.LBB0_787:
	s_add_u32 s4, s38, 0x80
	s_addc_u32 s5, s39, 0
	s_add_i32 s69, 0, 0x10000
	s_cmp_eq_u32 s68, 28
	s_cselect_b32 s5, s35, s5
	s_cselect_b32 s4, s34, s4
	s_cselect_b32 s45, s37, s31
	s_cselect_b32 s44, s36, s29
	s_add_i32 s74, 0, 0x14000
	v_lshl_add_u64 v[198:199], s[38:39], 0, v[152:153]
	s_add_i32 m0, s50, 0xc000
	s_nop 0
	global_load_lds_dwordx4 v[198:199], off
	v_lshl_add_u64 v[198:199], s[38:39], 0, v[150:151]
	s_add_i32 m0, s50, 0xe000
	s_nop 0
	global_load_lds_dwordx4 v[198:199], off
	v_add_u32_e32 v154, s69, v162
	v_add_u32_e32 v165, s74, v162
	ds_read_b128 v[132:135], v154
	ds_read_b128 v[136:139], v154 offset:1024
	ds_read_b128 v[140:143], v154 offset:2048
	ds_read_b128 v[154:157], v154 offset:3072
	ds_read_b128 v[158:161], v165
	ds_read_b128 v[166:169], v165 offset:1024
	ds_read_b128 v[170:173], v165 offset:2048
	ds_read_b128 v[174:177], v165 offset:3072
	ds_read_b128 v[178:181], v164
	ds_read_b128 v[182:185], v164 offset:1024
	ds_read_b128 v[186:189], v164 offset:2048
	ds_read_b128 v[190:193], v164 offset:3072
	ds_read_b128 v[194:197], v164 offset:4096
	ds_read_b128 v[224:227], v164 offset:5120
	ds_read_b128 v[228:231], v164 offset:6144
	ds_read_b128 v[238:241], v164 offset:7168
	s_waitcnt vmcnt(8)
	s_waitcnt lgkmcnt(0)
	s_barrier
	s_setprio 1
	s_waitcnt lgkmcnt(0)
	v_mfma_f32_16x16x32_bf16 v[128:131], v[132:135], v[178:181], v[128:131]
	v_mfma_f32_16x16x32_bf16 v[124:127], v[140:143], v[178:181], v[124:127]
	v_mfma_f32_16x16x32_bf16 v[120:123], v[132:135], v[186:189], v[120:123]
	v_mfma_f32_16x16x32_bf16 v[108:111], v[140:143], v[186:189], v[108:111]
	v_mfma_f32_16x16x32_bf16 v[104:107], v[132:135], v[194:197], v[104:107]
	v_mfma_f32_16x16x32_bf16 v[92:95], v[140:143], v[194:197], v[92:95]
	v_mfma_f32_16x16x32_bf16 v[88:91], v[132:135], v[228:231], v[88:91]
	v_mfma_f32_16x16x32_bf16 v[76:79], v[140:143], v[228:231], v[76:79]
	v_mfma_f32_16x16x32_bf16 v[128:131], v[136:139], v[182:185], v[128:131]
	v_mfma_f32_16x16x32_bf16 v[124:127], v[154:157], v[182:185], v[124:127]
	v_mfma_f32_16x16x32_bf16 v[120:123], v[136:139], v[190:193], v[120:123]
	v_mfma_f32_16x16x32_bf16 v[108:111], v[154:157], v[190:193], v[108:111]
	v_mfma_f32_16x16x32_bf16 v[104:107], v[136:139], v[224:227], v[104:107]
	v_mfma_f32_16x16x32_bf16 v[92:95], v[154:157], v[224:227], v[92:95]
	v_mfma_f32_16x16x32_bf16 v[88:91], v[136:139], v[238:241], v[88:91]
	v_mfma_f32_16x16x32_bf16 v[76:79], v[154:157], v[238:241], v[76:79]
	s_setprio 0
	s_setprio 1
	v_mfma_f32_16x16x32_bf16 v[116:119], v[158:161], v[178:181], v[116:119]
	v_mfma_f32_16x16x32_bf16 v[112:115], v[170:173], v[178:181], v[112:115]
	v_mfma_f32_16x16x32_bf16 v[100:103], v[158:161], v[186:189], v[100:103]
	v_mfma_f32_16x16x32_bf16 v[96:99], v[170:173], v[186:189], v[96:99]
	v_mfma_f32_16x16x32_bf16 v[84:87], v[158:161], v[194:197], v[84:87]
	v_mfma_f32_16x16x32_bf16 v[80:83], v[170:173], v[194:197], v[80:83]
	v_mfma_f32_16x16x32_bf16 v[72:75], v[158:161], v[228:231], v[72:75]
	v_mfma_f32_16x16x32_bf16 v[68:71], v[170:173], v[228:231], v[68:71]
	v_mfma_f32_16x16x32_bf16 v[116:119], v[166:169], v[182:185], v[116:119]
	v_mfma_f32_16x16x32_bf16 v[112:115], v[174:177], v[182:185], v[112:115]
	v_mfma_f32_16x16x32_bf16 v[100:103], v[166:169], v[190:193], v[100:103]
	v_mfma_f32_16x16x32_bf16 v[96:99], v[174:177], v[190:193], v[96:99]
	v_mfma_f32_16x16x32_bf16 v[84:87], v[166:169], v[224:227], v[84:87]
	v_mfma_f32_16x16x32_bf16 v[80:83], v[174:177], v[224:227], v[80:83]
	v_mfma_f32_16x16x32_bf16 v[72:75], v[166:169], v[238:241], v[72:75]
	v_mfma_f32_16x16x32_bf16 v[68:71], v[174:177], v[238:241], v[68:71]
	s_setprio 0
	s_barrier
	s_add_i32 s69, s69, s49
	v_lshl_add_u64 v[198:199], s[44:45], 0, v[34:35]
	s_mov_b32 m0, s69
	s_nop 0
	global_load_lds_dwordx4 v[198:199], off
	s_add_i32 m0, s69, 0x2000
	s_add_u32 s70, s44, 0x80000
	v_lshl_add_u64 v[212:213], s[44:45], 0, v[144:145]
	s_addc_u32 s71, s45, 0
	s_add_i32 s69, s74, s49
	global_load_lds_dwordx4 v[212:213], off
	v_lshl_add_u64 v[232:233], s[70:71], 0, v[34:35]
	s_mov_b32 m0, s69
	v_lshl_add_u64 v[242:243], s[4:5], 0, v[144:145]
	global_load_lds_dwordx4 v[232:233], off
	v_lshl_add_u64 v[232:233], s[70:71], 0, v[144:145]
	s_add_i32 m0, s69, 0x2000
	s_nop 0
	global_load_lds_dwordx4 v[232:233], off
	v_lshl_add_u64 v[232:233], s[4:5], 0, v[34:35]
	s_mov_b32 m0, s50
	s_nop 0
	global_load_lds_dwordx4 v[232:233], off
	s_mov_b32 m0, s51
	s_nop 0
	global_load_lds_dwordx4 v[242:243], off
	ds_read_b128 v[178:181], v164 offset:16384
	ds_read_b128 v[182:185], v164 offset:17408
	ds_read_b128 v[186:189], v164 offset:18432
	ds_read_b128 v[190:193], v164 offset:19456
	ds_read_b128 v[194:197], v164 offset:20480
	ds_read_b128 v[224:227], v164 offset:21504
	ds_read_b128 v[228:231], v164 offset:22528
	ds_read_b128 v[238:241], v164 offset:23552
	s_waitcnt vmcnt(8)
	s_waitcnt lgkmcnt(0)
	s_barrier
	s_setprio 1
	s_waitcnt lgkmcnt(0)
	v_mfma_f32_16x16x32_bf16 v[64:67], v[132:135], v[178:181], v[64:67]
	v_mfma_f32_16x16x32_bf16 v[60:63], v[140:143], v[178:181], v[60:63]
	v_mfma_f32_16x16x32_bf16 v[56:59], v[132:135], v[186:189], v[56:59]
	v_mfma_f32_16x16x32_bf16 v[44:47], v[140:143], v[186:189], v[44:47]
	v_mfma_f32_16x16x32_bf16 v[40:43], v[132:135], v[194:197], v[40:43]
	v_mfma_f32_16x16x32_bf16 v[26:29], v[140:143], v[194:197], v[26:29]
	v_mfma_f32_16x16x32_bf16 v[22:25], v[132:135], v[228:231], v[22:25]
	v_mfma_f32_16x16x32_bf16 v[10:13], v[140:143], v[228:231], v[10:13]
	v_mfma_f32_16x16x32_bf16 v[64:67], v[136:139], v[182:185], v[64:67]
	v_mfma_f32_16x16x32_bf16 v[60:63], v[154:157], v[182:185], v[60:63]
	v_mfma_f32_16x16x32_bf16 v[56:59], v[136:139], v[190:193], v[56:59]
	v_mfma_f32_16x16x32_bf16 v[44:47], v[154:157], v[190:193], v[44:47]
	v_mfma_f32_16x16x32_bf16 v[40:43], v[136:139], v[224:227], v[40:43]
	v_mfma_f32_16x16x32_bf16 v[26:29], v[154:157], v[224:227], v[26:29]
	v_mfma_f32_16x16x32_bf16 v[22:25], v[136:139], v[238:241], v[22:25]
	v_mfma_f32_16x16x32_bf16 v[10:13], v[154:157], v[238:241], v[10:13]
	s_setprio 0
	s_setprio 1
	v_mfma_f32_16x16x32_bf16 v[52:55], v[158:161], v[178:181], v[52:55]
	v_mfma_f32_16x16x32_bf16 v[48:51], v[170:173], v[178:181], v[48:51]
	v_mfma_f32_16x16x32_bf16 v[36:39], v[158:161], v[186:189], v[36:39]
	v_mfma_f32_16x16x32_bf16 v[30:33], v[170:173], v[186:189], v[30:33]
	v_mfma_f32_16x16x32_bf16 v[18:21], v[158:161], v[194:197], v[18:21]
	v_mfma_f32_16x16x32_bf16 v[14:17], v[170:173], v[194:197], v[14:17]
	v_mfma_f32_16x16x32_bf16 v[6:9], v[158:161], v[228:231], v[6:9]
	v_mfma_f32_16x16x32_bf16 v[2:5], v[170:173], v[228:231], v[2:5]
	v_mfma_f32_16x16x32_bf16 v[52:55], v[166:169], v[182:185], v[52:55]
	v_mfma_f32_16x16x32_bf16 v[48:51], v[174:177], v[182:185], v[48:51]
	v_mfma_f32_16x16x32_bf16 v[36:39], v[166:169], v[190:193], v[36:39]
	v_mfma_f32_16x16x32_bf16 v[30:33], v[174:177], v[190:193], v[30:33]
	v_mfma_f32_16x16x32_bf16 v[18:21], v[166:169], v[224:227], v[18:21]
	v_mfma_f32_16x16x32_bf16 v[14:17], v[174:177], v[224:227], v[14:17]
	v_mfma_f32_16x16x32_bf16 v[6:9], v[166:169], v[238:241], v[6:9]
	v_mfma_f32_16x16x32_bf16 v[2:5], v[174:177], v[238:241], v[2:5]
	s_setprio 0
	s_barrier
	s_add_i32 s69, 0, 0x18000
	s_add_i32 s70, 0, 0x1c000
	s_mov_b32 m0, s52
	v_lshl_add_u64 v[244:245], s[4:5], 0, v[148:149]
	global_load_lds_dwordx4 v[244:245], off
	v_lshl_add_u64 v[244:245], s[4:5], 0, v[146:147]
	s_mov_b32 m0, s53
	s_nop 0
	global_load_lds_dwordx4 v[244:245], off
	v_add_u32_e32 v154, s69, v162
	v_add_u32_e32 v165, s70, v162
	ds_read_b128 v[132:135], v154
	ds_read_b128 v[136:139], v154 offset:1024
	ds_read_b128 v[140:143], v154 offset:2048
	ds_read_b128 v[154:157], v154 offset:3072
	ds_read_b128 v[158:161], v165
	ds_read_b128 v[166:169], v165 offset:1024
	ds_read_b128 v[170:173], v165 offset:2048
	ds_read_b128 v[174:177], v165 offset:3072
	ds_read_b128 v[178:181], v164 offset:32768
	ds_read_b128 v[182:185], v164 offset:33792
	ds_read_b128 v[186:189], v164 offset:34816
	ds_read_b128 v[190:193], v164 offset:35840
	ds_read_b128 v[194:197], v164 offset:36864
	ds_read_b128 v[224:227], v164 offset:37888
	ds_read_b128 v[228:231], v164 offset:38912
	ds_read_b128 v[238:241], v164 offset:39936
	s_waitcnt vmcnt(8)
	s_waitcnt lgkmcnt(0)
	s_barrier
	s_setprio 1
	s_waitcnt lgkmcnt(0)
	v_mfma_f32_16x16x32_bf16 v[128:131], v[132:135], v[178:181], v[128:131]
	v_mfma_f32_16x16x32_bf16 v[124:127], v[140:143], v[178:181], v[124:127]
	v_mfma_f32_16x16x32_bf16 v[120:123], v[132:135], v[186:189], v[120:123]
	v_mfma_f32_16x16x32_bf16 v[108:111], v[140:143], v[186:189], v[108:111]
	v_mfma_f32_16x16x32_bf16 v[104:107], v[132:135], v[194:197], v[104:107]
	v_mfma_f32_16x16x32_bf16 v[92:95], v[140:143], v[194:197], v[92:95]
	v_mfma_f32_16x16x32_bf16 v[88:91], v[132:135], v[228:231], v[88:91]
	v_mfma_f32_16x16x32_bf16 v[76:79], v[140:143], v[228:231], v[76:79]
	v_mfma_f32_16x16x32_bf16 v[128:131], v[136:139], v[182:185], v[128:131]
	v_mfma_f32_16x16x32_bf16 v[124:127], v[154:157], v[182:185], v[124:127]
	v_mfma_f32_16x16x32_bf16 v[120:123], v[136:139], v[190:193], v[120:123]
	v_mfma_f32_16x16x32_bf16 v[108:111], v[154:157], v[190:193], v[108:111]
	v_mfma_f32_16x16x32_bf16 v[104:107], v[136:139], v[224:227], v[104:107]
	v_mfma_f32_16x16x32_bf16 v[92:95], v[154:157], v[224:227], v[92:95]
	v_mfma_f32_16x16x32_bf16 v[88:91], v[136:139], v[238:241], v[88:91]
	v_mfma_f32_16x16x32_bf16 v[76:79], v[154:157], v[238:241], v[76:79]
	s_setprio 0
	s_setprio 1
	v_mfma_f32_16x16x32_bf16 v[116:119], v[158:161], v[178:181], v[116:119]
	v_mfma_f32_16x16x32_bf16 v[112:115], v[170:173], v[178:181], v[112:115]
	v_mfma_f32_16x16x32_bf16 v[100:103], v[158:161], v[186:189], v[100:103]
	v_mfma_f32_16x16x32_bf16 v[96:99], v[170:173], v[186:189], v[96:99]
	v_mfma_f32_16x16x32_bf16 v[84:87], v[158:161], v[194:197], v[84:87]
	v_mfma_f32_16x16x32_bf16 v[80:83], v[170:173], v[194:197], v[80:83]
	v_mfma_f32_16x16x32_bf16 v[72:75], v[158:161], v[228:231], v[72:75]
	v_mfma_f32_16x16x32_bf16 v[68:71], v[170:173], v[228:231], v[68:71]
	v_mfma_f32_16x16x32_bf16 v[116:119], v[166:169], v[182:185], v[116:119]
	v_mfma_f32_16x16x32_bf16 v[112:115], v[174:177], v[182:185], v[112:115]
	v_mfma_f32_16x16x32_bf16 v[100:103], v[166:169], v[190:193], v[100:103]
	v_mfma_f32_16x16x32_bf16 v[96:99], v[174:177], v[190:193], v[96:99]
	v_mfma_f32_16x16x32_bf16 v[84:87], v[166:169], v[224:227], v[84:87]
	v_mfma_f32_16x16x32_bf16 v[80:83], v[174:177], v[224:227], v[80:83]
	v_mfma_f32_16x16x32_bf16 v[72:75], v[166:169], v[238:241], v[72:75]
	v_mfma_f32_16x16x32_bf16 v[68:71], v[174:177], v[238:241], v[68:71]
	s_setprio 0
	s_barrier
	s_add_i32 s4, s69, s49
	v_lshl_add_u64 v[198:199], v[198:199], 0, s[78:79]
	s_mov_b32 m0, s4
	s_nop 0
	global_load_lds_dwordx4 v[198:199], off
	s_add_i32 m0, s4, 0x2000
	s_add_u32 s4, s44, 0x80080
	v_lshl_add_u64 v[198:199], v[212:213], 0, s[78:79]
	s_addc_u32 s5, s45, 0
	s_add_i32 s44, s70, s49
	global_load_lds_dwordx4 v[198:199], off
	v_lshl_add_u64 v[198:199], s[4:5], 0, v[34:35]
	s_mov_b32 m0, s44
	s_nop 0
	global_load_lds_dwordx4 v[198:199], off
	v_lshl_add_u64 v[198:199], s[4:5], 0, v[144:145]
	s_add_i32 m0, s44, 0x2000
	s_nop 0
	global_load_lds_dwordx4 v[198:199], off
	v_lshl_add_u64 v[198:199], v[232:233], 0, s[78:79]
	s_mov_b32 m0, s54
	s_nop 0
	global_load_lds_dwordx4 v[198:199], off
	v_lshl_add_u64 v[198:199], v[242:243], 0, s[78:79]
	s_mov_b32 m0, s55
	s_nop 0
	global_load_lds_dwordx4 v[198:199], off
	ds_read_b128 v[178:181], v164 offset:49152
	ds_read_b128 v[182:185], v164 offset:50176
	ds_read_b128 v[186:189], v164 offset:51200
	ds_read_b128 v[190:193], v164 offset:52224
	ds_read_b128 v[194:197], v164 offset:53248
	ds_read_b128 v[224:227], v164 offset:54272
	ds_read_b128 v[228:231], v164 offset:55296
	ds_read_b128 v[238:241], v164 offset:56320
	s_waitcnt vmcnt(8)
	s_waitcnt lgkmcnt(0)
	s_barrier
	s_setprio 1
	s_waitcnt lgkmcnt(0)
	v_mfma_f32_16x16x32_bf16 v[64:67], v[132:135], v[178:181], v[64:67]
	v_mfma_f32_16x16x32_bf16 v[60:63], v[140:143], v[178:181], v[60:63]
	v_mfma_f32_16x16x32_bf16 v[56:59], v[132:135], v[186:189], v[56:59]
	v_mfma_f32_16x16x32_bf16 v[44:47], v[140:143], v[186:189], v[44:47]
	v_mfma_f32_16x16x32_bf16 v[40:43], v[132:135], v[194:197], v[40:43]
	v_mfma_f32_16x16x32_bf16 v[26:29], v[140:143], v[194:197], v[26:29]
	v_mfma_f32_16x16x32_bf16 v[22:25], v[132:135], v[228:231], v[22:25]
	v_mfma_f32_16x16x32_bf16 v[10:13], v[140:143], v[228:231], v[10:13]
	v_mfma_f32_16x16x32_bf16 v[64:67], v[136:139], v[182:185], v[64:67]
	v_mfma_f32_16x16x32_bf16 v[60:63], v[154:157], v[182:185], v[60:63]
	v_mfma_f32_16x16x32_bf16 v[56:59], v[136:139], v[190:193], v[56:59]
	v_mfma_f32_16x16x32_bf16 v[44:47], v[154:157], v[190:193], v[44:47]
	v_mfma_f32_16x16x32_bf16 v[40:43], v[136:139], v[224:227], v[40:43]
	v_mfma_f32_16x16x32_bf16 v[26:29], v[154:157], v[224:227], v[26:29]
	v_mfma_f32_16x16x32_bf16 v[22:25], v[136:139], v[238:241], v[22:25]
	v_mfma_f32_16x16x32_bf16 v[10:13], v[154:157], v[238:241], v[10:13]
	s_setprio 0
	s_setprio 1
	v_mfma_f32_16x16x32_bf16 v[52:55], v[158:161], v[178:181], v[52:55]
	v_mfma_f32_16x16x32_bf16 v[48:51], v[170:173], v[178:181], v[48:51]
	v_mfma_f32_16x16x32_bf16 v[36:39], v[158:161], v[186:189], v[36:39]
	v_mfma_f32_16x16x32_bf16 v[30:33], v[170:173], v[186:189], v[30:33]
	v_mfma_f32_16x16x32_bf16 v[18:21], v[158:161], v[194:197], v[18:21]
	v_mfma_f32_16x16x32_bf16 v[14:17], v[170:173], v[194:197], v[14:17]
	v_mfma_f32_16x16x32_bf16 v[6:9], v[158:161], v[228:231], v[6:9]
	v_mfma_f32_16x16x32_bf16 v[2:5], v[170:173], v[228:231], v[2:5]
	v_mfma_f32_16x16x32_bf16 v[52:55], v[166:169], v[182:185], v[52:55]
	v_mfma_f32_16x16x32_bf16 v[48:51], v[174:177], v[182:185], v[48:51]
	v_mfma_f32_16x16x32_bf16 v[36:39], v[166:169], v[190:193], v[36:39]
	v_mfma_f32_16x16x32_bf16 v[30:33], v[174:177], v[190:193], v[30:33]
	v_mfma_f32_16x16x32_bf16 v[18:21], v[166:169], v[224:227], v[18:21]
	v_mfma_f32_16x16x32_bf16 v[14:17], v[174:177], v[224:227], v[14:17]
	v_mfma_f32_16x16x32_bf16 v[6:9], v[166:169], v[238:241], v[6:9]
	v_mfma_f32_16x16x32_bf16 v[2:5], v[174:177], v[238:241], v[2:5]
	s_setprio 0
	s_barrier
	s_add_i32 s68, s68, 2
	s_add_u32 s29, s29, 0x100
	s_addc_u32 s31, s31, 0
	s_add_u32 s38, s38, 0x100
	s_addc_u32 s39, s39, 0
	s_cmp_gt_u32 s68, 29
	s_cbranch_scc0 .LBB0_787
	s_and_b64 vcc, exec, s[26:27]
	s_cbranch_vccz .LBB0_790
	s_barrier

.LBB0_899:
	s_add_u32 s4, s36, 0x80
	s_addc_u32 s5, s37, 0
	s_add_i32 s68, 0, 0x10000
	s_cmp_eq_u32 s65, 28
	s_cselect_b32 s39, s31, s5
	s_cselect_b32 s38, s30, s4
	s_cselect_b32 s5, s35, s64
	s_cselect_b32 s4, s34, s29
	v_lshl_add_u64 v[132:133], s[36:37], 0, v[78:79]
	s_add_i32 m0, s45, 0xc000
	s_nop 0
	global_load_lds_dwordx4 v[132:133], off
	v_lshl_add_u64 v[132:133], s[36:37], 0, v[76:77]
	s_add_i32 m0, s45, 0xe000
	s_nop 0
	global_load_lds_dwordx4 v[132:133], off
	v_add_u32_e32 v83, s68, v81
	ds_read_b128 v[84:87], v83
	ds_read_b128 v[88:91], v83 offset:1024
	ds_read_b128 v[92:95], v83 offset:2048
	ds_read_b128 v[96:99], v83 offset:3072
	ds_read_b128 v[100:103], v82
	ds_read_b128 v[104:107], v82 offset:1024
	ds_read_b128 v[108:111], v82 offset:2048
	ds_read_b128 v[112:115], v82 offset:3072
	ds_read_b128 v[116:119], v82 offset:4096
	ds_read_b128 v[120:123], v82 offset:5120
	ds_read_b128 v[124:127], v82 offset:6144
	ds_read_b128 v[128:131], v82 offset:7168
	s_waitcnt vmcnt(8)
	s_waitcnt lgkmcnt(0)
	s_barrier
	s_setprio 1
	s_waitcnt lgkmcnt(0)
	v_mfma_f32_16x16x32_bf16 v[64:67], v[84:87], v[100:103], v[64:67]
	v_mfma_f32_16x16x32_bf16 v[60:63], v[92:95], v[100:103], v[60:63]
	v_mfma_f32_16x16x32_bf16 v[56:59], v[84:87], v[108:111], v[56:59]
	v_mfma_f32_16x16x32_bf16 v[52:55], v[92:95], v[108:111], v[52:55]
	v_mfma_f32_16x16x32_bf16 v[48:51], v[84:87], v[116:119], v[48:51]
	v_mfma_f32_16x16x32_bf16 v[44:47], v[92:95], v[116:119], v[44:47]
	v_mfma_f32_16x16x32_bf16 v[40:43], v[84:87], v[124:127], v[40:43]
	v_mfma_f32_16x16x32_bf16 v[36:39], v[92:95], v[124:127], v[36:39]
	v_mfma_f32_16x16x32_bf16 v[64:67], v[88:91], v[104:107], v[64:67]
	v_mfma_f32_16x16x32_bf16 v[60:63], v[96:99], v[104:107], v[60:63]
	v_mfma_f32_16x16x32_bf16 v[56:59], v[88:91], v[112:115], v[56:59]
	v_mfma_f32_16x16x32_bf16 v[52:55], v[96:99], v[112:115], v[52:55]
	v_mfma_f32_16x16x32_bf16 v[48:51], v[88:91], v[120:123], v[48:51]
	v_mfma_f32_16x16x32_bf16 v[44:47], v[96:99], v[120:123], v[44:47]
	v_mfma_f32_16x16x32_bf16 v[40:43], v[88:91], v[128:131], v[40:43]
	v_mfma_f32_16x16x32_bf16 v[36:39], v[96:99], v[128:131], v[36:39]
	s_setprio 0
	s_setprio 1
	s_setprio 0
	s_barrier
	s_add_i32 s68, s68, s44
	v_lshl_add_u64 v[132:133], s[4:5], 0, v[34:35]
	s_mov_b32 m0, s68
	s_nop 0
	global_load_lds_dwordx4 v[132:133], off
	s_add_i32 m0, s68, 0x2000
	s_add_u32 s68, s4, 0x80000
	v_lshl_add_u64 v[134:135], s[4:5], 0, v[68:69]
	s_addc_u32 s69, s5, 0
	global_load_lds_dwordx4 v[134:135], off
	v_lshl_add_u64 v[136:137], s[68:69], 0, v[34:35]
	s_mov_b32 m0, s46
	v_lshl_add_u64 v[138:139], s[38:39], 0, v[68:69]
	global_load_lds_dwordx4 v[136:137], off
	v_lshl_add_u64 v[136:137], s[68:69], 0, v[68:69]
	s_mov_b32 m0, s47
	s_nop 0
	global_load_lds_dwordx4 v[136:137], off
	v_lshl_add_u64 v[136:137], s[38:39], 0, v[34:35]
	s_mov_b32 m0, s45
	s_nop 0
	global_load_lds_dwordx4 v[136:137], off
	s_mov_b32 m0, s48
	s_nop 0
	global_load_lds_dwordx4 v[138:139], off
	ds_read_b128 v[100:103], v82 offset:16384
	ds_read_b128 v[104:107], v82 offset:17408
	ds_read_b128 v[108:111], v82 offset:18432
	ds_read_b128 v[112:115], v82 offset:19456
	ds_read_b128 v[116:119], v82 offset:20480
	ds_read_b128 v[120:123], v82 offset:21504
	ds_read_b128 v[124:127], v82 offset:22528
	ds_read_b128 v[128:131], v82 offset:23552
	s_waitcnt vmcnt(8)
	s_waitcnt lgkmcnt(0)
	s_barrier
	s_setprio 1
	s_waitcnt lgkmcnt(0)
	v_mfma_f32_16x16x32_bf16 v[30:33], v[84:87], v[100:103], v[30:33]
	v_mfma_f32_16x16x32_bf16 v[26:29], v[92:95], v[100:103], v[26:29]
	v_mfma_f32_16x16x32_bf16 v[22:25], v[84:87], v[108:111], v[22:25]
	v_mfma_f32_16x16x32_bf16 v[18:21], v[92:95], v[108:111], v[18:21]
	v_mfma_f32_16x16x32_bf16 v[14:17], v[84:87], v[116:119], v[14:17]
	v_mfma_f32_16x16x32_bf16 v[10:13], v[92:95], v[116:119], v[10:13]
	v_mfma_f32_16x16x32_bf16 v[6:9], v[84:87], v[124:127], v[6:9]
	v_mfma_f32_16x16x32_bf16 v[2:5], v[92:95], v[124:127], v[2:5]
	v_mfma_f32_16x16x32_bf16 v[30:33], v[88:91], v[104:107], v[30:33]
	v_mfma_f32_16x16x32_bf16 v[26:29], v[96:99], v[104:107], v[26:29]
	v_mfma_f32_16x16x32_bf16 v[22:25], v[88:91], v[112:115], v[22:25]
	v_mfma_f32_16x16x32_bf16 v[18:21], v[96:99], v[112:115], v[18:21]
	v_mfma_f32_16x16x32_bf16 v[14:17], v[88:91], v[120:123], v[14:17]
	v_mfma_f32_16x16x32_bf16 v[10:13], v[96:99], v[120:123], v[10:13]
	v_mfma_f32_16x16x32_bf16 v[6:9], v[88:91], v[128:131], v[6:9]
	v_mfma_f32_16x16x32_bf16 v[2:5], v[96:99], v[128:131], v[2:5]
	s_setprio 0
	s_setprio 1
	s_setprio 0
	s_barrier
	s_add_i32 s68, 0, 0x18000
	s_mov_b32 m0, s49
	v_lshl_add_u64 v[140:141], s[38:39], 0, v[72:73]
	global_load_lds_dwordx4 v[140:141], off
	v_lshl_add_u64 v[140:141], s[38:39], 0, v[70:71]
	s_mov_b32 m0, s50
	s_nop 0
	global_load_lds_dwordx4 v[140:141], off
	v_add_u32_e32 v83, s68, v81
	ds_read_b128 v[84:87], v83
	ds_read_b128 v[88:91], v83 offset:1024
	ds_read_b128 v[92:95], v83 offset:2048
	ds_read_b128 v[96:99], v83 offset:3072
	ds_read_b128 v[100:103], v82 offset:32768
	ds_read_b128 v[104:107], v82 offset:33792
	ds_read_b128 v[108:111], v82 offset:34816
	ds_read_b128 v[112:115], v82 offset:35840
	ds_read_b128 v[116:119], v82 offset:36864
	ds_read_b128 v[120:123], v82 offset:37888
	ds_read_b128 v[124:127], v82 offset:38912
	ds_read_b128 v[128:131], v82 offset:39936
	s_waitcnt vmcnt(8)
	s_waitcnt lgkmcnt(0)
	s_barrier
	s_setprio 1
	s_waitcnt lgkmcnt(0)
	v_mfma_f32_16x16x32_bf16 v[64:67], v[84:87], v[100:103], v[64:67]
	v_mfma_f32_16x16x32_bf16 v[60:63], v[92:95], v[100:103], v[60:63]
	v_mfma_f32_16x16x32_bf16 v[56:59], v[84:87], v[108:111], v[56:59]
	v_mfma_f32_16x16x32_bf16 v[52:55], v[92:95], v[108:111], v[52:55]
	v_mfma_f32_16x16x32_bf16 v[48:51], v[84:87], v[116:119], v[48:51]
	v_mfma_f32_16x16x32_bf16 v[44:47], v[92:95], v[116:119], v[44:47]
	v_mfma_f32_16x16x32_bf16 v[40:43], v[84:87], v[124:127], v[40:43]
	v_mfma_f32_16x16x32_bf16 v[36:39], v[92:95], v[124:127], v[36:39]
	v_mfma_f32_16x16x32_bf16 v[64:67], v[88:91], v[104:107], v[64:67]
	v_mfma_f32_16x16x32_bf16 v[60:63], v[96:99], v[104:107], v[60:63]
	v_mfma_f32_16x16x32_bf16 v[56:59], v[88:91], v[112:115], v[56:59]
	v_mfma_f32_16x16x32_bf16 v[52:55], v[96:99], v[112:115], v[52:55]
	v_mfma_f32_16x16x32_bf16 v[48:51], v[88:91], v[120:123], v[48:51]
	v_mfma_f32_16x16x32_bf16 v[44:47], v[96:99], v[120:123], v[44:47]
	v_mfma_f32_16x16x32_bf16 v[40:43], v[88:91], v[128:131], v[40:43]
	v_mfma_f32_16x16x32_bf16 v[36:39], v[96:99], v[128:131], v[36:39]
	s_setprio 0
	s_setprio 1
	s_setprio 0
	s_barrier
	s_add_i32 s38, s68, s44
	v_lshl_add_u64 v[132:133], v[132:133], 0, s[78:79]
	s_mov_b32 m0, s38
	s_nop 0
	global_load_lds_dwordx4 v[132:133], off
	s_add_i32 m0, s38, 0x2000
	s_add_u32 s4, s4, 0x80080
	v_lshl_add_u64 v[132:133], v[134:135], 0, s[78:79]
	s_addc_u32 s5, s5, 0
	global_load_lds_dwordx4 v[132:133], off
	v_lshl_add_u64 v[132:133], s[4:5], 0, v[34:35]
	s_mov_b32 m0, s53
	s_nop 0
	global_load_lds_dwordx4 v[132:133], off
	v_lshl_add_u64 v[132:133], s[4:5], 0, v[68:69]
	s_mov_b32 m0, s54
	s_nop 0
	global_load_lds_dwordx4 v[132:133], off
	v_lshl_add_u64 v[132:133], v[136:137], 0, s[78:79]
	s_mov_b32 m0, s51
	s_nop 0
	global_load_lds_dwordx4 v[132:133], off
	v_lshl_add_u64 v[132:133], v[138:139], 0, s[78:79]
	s_mov_b32 m0, s52
	s_nop 0
	global_load_lds_dwordx4 v[132:133], off
	ds_read_b128 v[100:103], v82 offset:49152
	ds_read_b128 v[104:107], v82 offset:50176
	ds_read_b128 v[108:111], v82 offset:51200
	ds_read_b128 v[112:115], v82 offset:52224
	ds_read_b128 v[116:119], v82 offset:53248
	ds_read_b128 v[120:123], v82 offset:54272
	ds_read_b128 v[124:127], v82 offset:55296
	ds_read_b128 v[128:131], v82 offset:56320
	s_waitcnt vmcnt(8)
	s_waitcnt lgkmcnt(0)
	s_barrier
	s_setprio 1
	s_waitcnt lgkmcnt(0)
	v_mfma_f32_16x16x32_bf16 v[30:33], v[84:87], v[100:103], v[30:33]
	v_mfma_f32_16x16x32_bf16 v[26:29], v[92:95], v[100:103], v[26:29]
	v_mfma_f32_16x16x32_bf16 v[22:25], v[84:87], v[108:111], v[22:25]
	v_mfma_f32_16x16x32_bf16 v[18:21], v[92:95], v[108:111], v[18:21]
	v_mfma_f32_16x16x32_bf16 v[14:17], v[84:87], v[116:119], v[14:17]
	v_mfma_f32_16x16x32_bf16 v[10:13], v[92:95], v[116:119], v[10:13]
	v_mfma_f32_16x16x32_bf16 v[6:9], v[84:87], v[124:127], v[6:9]
	v_mfma_f32_16x16x32_bf16 v[2:5], v[92:95], v[124:127], v[2:5]
	v_mfma_f32_16x16x32_bf16 v[30:33], v[88:91], v[104:107], v[30:33]
	v_mfma_f32_16x16x32_bf16 v[26:29], v[96:99], v[104:107], v[26:29]
	v_mfma_f32_16x16x32_bf16 v[22:25], v[88:91], v[112:115], v[22:25]
	v_mfma_f32_16x16x32_bf16 v[18:21], v[96:99], v[112:115], v[18:21]
	v_mfma_f32_16x16x32_bf16 v[14:17], v[88:91], v[120:123], v[14:17]
	v_mfma_f32_16x16x32_bf16 v[10:13], v[96:99], v[120:123], v[10:13]
	v_mfma_f32_16x16x32_bf16 v[6:9], v[88:91], v[128:131], v[6:9]
	v_mfma_f32_16x16x32_bf16 v[2:5], v[96:99], v[128:131], v[2:5]
	s_setprio 0
	s_setprio 1
	s_setprio 0
	s_barrier
	s_add_i32 s65, s65, 2
	s_add_u32 s29, s29, 0x100
	s_addc_u32 s64, s64, 0
	s_add_u32 s36, s36, 0x100
	s_addc_u32 s37, s37, 0
	s_cmp_gt_u32 s65, 29
	s_cbranch_scc0 .LBB0_899
	s_and_b64 vcc, exec, s[24:25]
	s_cbranch_vccz .LBB0_903
	s_barrier
	s_andn2_b64 vcc, exec, s[26:27]
	s_cbranch_vccz .LBB0_904

.LBB0_1199:
	s_add_u32 s4, s34, 0x80
	s_addc_u32 s5, s35, 0
	s_add_i32 s53, 0, 0x10000
	s_cmp_eq_u32 s52, 4
	s_cselect_b32 s5, s27, s5
	s_cselect_b32 s4, s26, s4
	s_cselect_b32 s37, s29, s51
	s_cselect_b32 s36, s28, s50
	s_add_i32 s56, 0, 0x14000
	v_lshl_add_u64 v[148:149], s[34:35], 0, v[146:147]
	s_add_i32 m0, s41, 0xc000
	s_nop 0
	global_load_lds_dwordx4 v[148:149], off
	v_lshl_add_u64 v[148:149], s[34:35], 0, v[144:145]
	s_add_i32 m0, s41, 0xe000
	s_nop 0
	global_load_lds_dwordx4 v[148:149], off
	v_add_u32_e32 v34, s53, v1
	ds_read_b128 v[154:157], v34
	ds_read_b128 v[158:161], v34 offset:1024
	ds_read_b128 v[162:165], v34 offset:2048
	ds_read_b128 v[166:169], v34 offset:3072
	v_add_u32_e32 v34, s56, v1
	ds_read_b128 v[170:173], v34
	ds_read_b128 v[174:177], v34 offset:1024
	ds_read_b128 v[178:181], v34 offset:2048
	ds_read_b128 v[182:185], v34 offset:3072
	ds_read_b128 v[186:189], v152
	ds_read_b128 v[190:193], v152 offset:1024
	ds_read_b128 v[194:197], v152 offset:2048
	ds_read_b128 v[224:227], v152 offset:3072
	ds_read_b128 v[228:231], v152 offset:4096
	ds_read_b128 v[238:241], v152 offset:5120
	ds_read_b128 v[242:245], v152 offset:6144
	ds_read_b128 v[246:249], v152 offset:7168
	s_waitcnt vmcnt(8)
	s_waitcnt lgkmcnt(0)
	s_barrier
	s_setprio 1
	s_waitcnt lgkmcnt(0)
	v_mfma_f32_16x16x32_bf16 v[128:131], v[154:157], v[186:189], v[128:131]
	v_mfma_f32_16x16x32_bf16 v[124:127], v[162:165], v[186:189], v[124:127]
	v_mfma_f32_16x16x32_bf16 v[116:119], v[154:157], v[194:197], v[116:119]
	v_mfma_f32_16x16x32_bf16 v[108:111], v[162:165], v[194:197], v[108:111]
	v_mfma_f32_16x16x32_bf16 v[100:103], v[154:157], v[228:231], v[100:103]
	v_mfma_f32_16x16x32_bf16 v[92:95], v[162:165], v[228:231], v[92:95]
	v_mfma_f32_16x16x32_bf16 v[84:87], v[154:157], v[242:245], v[84:87]
	v_mfma_f32_16x16x32_bf16 v[76:79], v[162:165], v[242:245], v[76:79]
	v_mfma_f32_16x16x32_bf16 v[128:131], v[158:161], v[190:193], v[128:131]
	v_mfma_f32_16x16x32_bf16 v[124:127], v[166:169], v[190:193], v[124:127]
	v_mfma_f32_16x16x32_bf16 v[116:119], v[158:161], v[224:227], v[116:119]
	v_mfma_f32_16x16x32_bf16 v[108:111], v[166:169], v[224:227], v[108:111]
	v_mfma_f32_16x16x32_bf16 v[100:103], v[158:161], v[238:241], v[100:103]
	v_mfma_f32_16x16x32_bf16 v[92:95], v[166:169], v[238:241], v[92:95]
	v_mfma_f32_16x16x32_bf16 v[84:87], v[158:161], v[246:249], v[84:87]
	v_mfma_f32_16x16x32_bf16 v[76:79], v[166:169], v[246:249], v[76:79]
	s_setprio 0
	s_setprio 1
	v_mfma_f32_16x16x32_bf16 v[120:123], v[170:173], v[186:189], v[120:123]
	v_mfma_f32_16x16x32_bf16 v[112:115], v[178:181], v[186:189], v[112:115]
	v_mfma_f32_16x16x32_bf16 v[104:107], v[170:173], v[194:197], v[104:107]
	v_mfma_f32_16x16x32_bf16 v[96:99], v[178:181], v[194:197], v[96:99]
	v_mfma_f32_16x16x32_bf16 v[88:91], v[170:173], v[228:231], v[88:91]
	v_mfma_f32_16x16x32_bf16 v[80:83], v[178:181], v[228:231], v[80:83]
	v_mfma_f32_16x16x32_bf16 v[72:75], v[170:173], v[242:245], v[72:75]
	v_mfma_f32_16x16x32_bf16 v[68:71], v[178:181], v[242:245], v[68:71]
	v_mfma_f32_16x16x32_bf16 v[120:123], v[174:177], v[190:193], v[120:123]
	v_mfma_f32_16x16x32_bf16 v[112:115], v[182:185], v[190:193], v[112:115]
	v_mfma_f32_16x16x32_bf16 v[104:107], v[174:177], v[224:227], v[104:107]
	v_mfma_f32_16x16x32_bf16 v[96:99], v[182:185], v[224:227], v[96:99]
	v_mfma_f32_16x16x32_bf16 v[88:91], v[174:177], v[238:241], v[88:91]
	v_mfma_f32_16x16x32_bf16 v[80:83], v[182:185], v[238:241], v[80:83]
	v_mfma_f32_16x16x32_bf16 v[72:75], v[174:177], v[246:249], v[72:75]
	v_mfma_f32_16x16x32_bf16 v[68:71], v[182:185], v[246:249], v[68:71]
	s_setprio 0
	s_barrier
	s_add_i32 s53, s53, s14
	v_lshl_add_u64 v[148:149], s[36:37], 0, v[138:139]
	s_mov_b32 m0, s53
	s_nop 0
	global_load_lds_dwordx4 v[148:149], off
	s_add_i32 m0, s53, 0x2000
	s_add_u32 s54, s36, 0x20000
	v_lshl_add_u64 v[198:199], s[36:37], 0, v[132:133]
	s_addc_u32 s55, s37, 0
	s_add_i32 s53, s56, s14
	global_load_lds_dwordx4 v[198:199], off
	v_lshl_add_u64 v[208:209], s[54:55], 0, v[138:139]
	s_mov_b32 m0, s53
	v_lshl_add_u64 v[212:213], s[4:5], 0, v[134:135]
	global_load_lds_dwordx4 v[208:209], off
	v_lshl_add_u64 v[208:209], s[54:55], 0, v[132:133]
	s_add_i32 m0, s53, 0x2000
	s_nop 0
	global_load_lds_dwordx4 v[208:209], off
	v_lshl_add_u64 v[208:209], s[4:5], 0, v[140:141]
	s_mov_b32 m0, s41
	s_nop 0
	global_load_lds_dwordx4 v[208:209], off
	s_mov_b32 m0, s42
	s_nop 0
	global_load_lds_dwordx4 v[212:213], off
	ds_read_b128 v[186:189], v152 offset:16384
	ds_read_b128 v[190:193], v152 offset:17408
	ds_read_b128 v[194:197], v152 offset:18432
	ds_read_b128 v[224:227], v152 offset:19456
	ds_read_b128 v[228:231], v152 offset:20480
	ds_read_b128 v[238:241], v152 offset:21504
	ds_read_b128 v[242:245], v152 offset:22528
	ds_read_b128 v[246:249], v152 offset:23552
	s_waitcnt vmcnt(8)
	s_waitcnt lgkmcnt(0)
	s_barrier
	s_setprio 1
	s_waitcnt lgkmcnt(0)
	v_mfma_f32_16x16x32_bf16 v[64:67], v[154:157], v[186:189], v[64:67]
	v_mfma_f32_16x16x32_bf16 v[60:63], v[162:165], v[186:189], v[60:63]
	v_mfma_f32_16x16x32_bf16 v[52:55], v[154:157], v[194:197], v[52:55]
	v_mfma_f32_16x16x32_bf16 v[44:47], v[162:165], v[194:197], v[44:47]
	v_mfma_f32_16x16x32_bf16 v[36:39], v[154:157], v[228:231], v[36:39]
	v_mfma_f32_16x16x32_bf16 v[26:29], v[162:165], v[228:231], v[26:29]
	v_mfma_f32_16x16x32_bf16 v[18:21], v[154:157], v[242:245], v[18:21]
	v_mfma_f32_16x16x32_bf16 v[10:13], v[162:165], v[242:245], v[10:13]
	v_mfma_f32_16x16x32_bf16 v[64:67], v[158:161], v[190:193], v[64:67]
	v_mfma_f32_16x16x32_bf16 v[60:63], v[166:169], v[190:193], v[60:63]
	v_mfma_f32_16x16x32_bf16 v[52:55], v[158:161], v[224:227], v[52:55]
	v_mfma_f32_16x16x32_bf16 v[44:47], v[166:169], v[224:227], v[44:47]
	v_mfma_f32_16x16x32_bf16 v[36:39], v[158:161], v[238:241], v[36:39]
	v_mfma_f32_16x16x32_bf16 v[26:29], v[166:169], v[238:241], v[26:29]
	v_mfma_f32_16x16x32_bf16 v[18:21], v[158:161], v[246:249], v[18:21]
	v_mfma_f32_16x16x32_bf16 v[10:13], v[166:169], v[246:249], v[10:13]
	s_setprio 0
	s_setprio 1
	v_mfma_f32_16x16x32_bf16 v[56:59], v[170:173], v[186:189], v[56:59]
	v_mfma_f32_16x16x32_bf16 v[48:51], v[178:181], v[186:189], v[48:51]
	v_mfma_f32_16x16x32_bf16 v[40:43], v[170:173], v[194:197], v[40:43]
	v_mfma_f32_16x16x32_bf16 v[30:33], v[178:181], v[194:197], v[30:33]
	v_mfma_f32_16x16x32_bf16 v[22:25], v[170:173], v[228:231], v[22:25]
	v_mfma_f32_16x16x32_bf16 v[14:17], v[178:181], v[228:231], v[14:17]
	v_mfma_f32_16x16x32_bf16 v[6:9], v[170:173], v[242:245], v[6:9]
	v_mfma_f32_16x16x32_bf16 v[2:5], v[178:181], v[242:245], v[2:5]
	v_mfma_f32_16x16x32_bf16 v[56:59], v[174:177], v[190:193], v[56:59]
	v_mfma_f32_16x16x32_bf16 v[48:51], v[182:185], v[190:193], v[48:51]
	v_mfma_f32_16x16x32_bf16 v[40:43], v[174:177], v[224:227], v[40:43]
	v_mfma_f32_16x16x32_bf16 v[30:33], v[182:185], v[224:227], v[30:33]
	v_mfma_f32_16x16x32_bf16 v[22:25], v[174:177], v[238:241], v[22:25]
	v_mfma_f32_16x16x32_bf16 v[14:17], v[182:185], v[238:241], v[14:17]
	v_mfma_f32_16x16x32_bf16 v[6:9], v[174:177], v[246:249], v[6:9]
	v_mfma_f32_16x16x32_bf16 v[2:5], v[182:185], v[246:249], v[2:5]
	s_setprio 0
	s_barrier
	s_add_i32 s53, 0, 0x18000
	s_add_i32 s54, 0, 0x1c000
	s_mov_b32 m0, s43
	v_lshl_add_u64 v[232:233], s[4:5], 0, v[142:143]
	global_load_lds_dwordx4 v[232:233], off
	v_lshl_add_u64 v[232:233], s[4:5], 0, v[136:137]
	s_mov_b32 m0, s44
	s_nop 0
	global_load_lds_dwordx4 v[232:233], off
	v_add_u32_e32 v34, s53, v1
	ds_read_b128 v[154:157], v34
	ds_read_b128 v[158:161], v34 offset:1024
	ds_read_b128 v[162:165], v34 offset:2048
	ds_read_b128 v[166:169], v34 offset:3072
	v_add_u32_e32 v34, s54, v1
	ds_read_b128 v[170:173], v34
	ds_read_b128 v[174:177], v34 offset:1024
	ds_read_b128 v[178:181], v34 offset:2048
	ds_read_b128 v[182:185], v34 offset:3072
	ds_read_b128 v[186:189], v152 offset:32768
	ds_read_b128 v[190:193], v152 offset:33792
	ds_read_b128 v[194:197], v152 offset:34816
	ds_read_b128 v[224:227], v152 offset:35840
	ds_read_b128 v[228:231], v152 offset:36864
	ds_read_b128 v[238:241], v152 offset:37888
	ds_read_b128 v[242:245], v152 offset:38912
	ds_read_b128 v[246:249], v152 offset:39936
	s_waitcnt vmcnt(8)
	s_waitcnt lgkmcnt(0)
	s_barrier
	s_setprio 1
	s_waitcnt lgkmcnt(0)
	v_mfma_f32_16x16x32_bf16 v[128:131], v[154:157], v[186:189], v[128:131]
	v_mfma_f32_16x16x32_bf16 v[124:127], v[162:165], v[186:189], v[124:127]
	v_mfma_f32_16x16x32_bf16 v[116:119], v[154:157], v[194:197], v[116:119]
	v_mfma_f32_16x16x32_bf16 v[108:111], v[162:165], v[194:197], v[108:111]
	v_mfma_f32_16x16x32_bf16 v[100:103], v[154:157], v[228:231], v[100:103]
	v_mfma_f32_16x16x32_bf16 v[92:95], v[162:165], v[228:231], v[92:95]
	v_mfma_f32_16x16x32_bf16 v[84:87], v[154:157], v[242:245], v[84:87]
	v_mfma_f32_16x16x32_bf16 v[76:79], v[162:165], v[242:245], v[76:79]
	v_mfma_f32_16x16x32_bf16 v[128:131], v[158:161], v[190:193], v[128:131]
	v_mfma_f32_16x16x32_bf16 v[124:127], v[166:169], v[190:193], v[124:127]
	v_mfma_f32_16x16x32_bf16 v[116:119], v[158:161], v[224:227], v[116:119]
	v_mfma_f32_16x16x32_bf16 v[108:111], v[166:169], v[224:227], v[108:111]
	v_mfma_f32_16x16x32_bf16 v[100:103], v[158:161], v[238:241], v[100:103]
	v_mfma_f32_16x16x32_bf16 v[92:95], v[166:169], v[238:241], v[92:95]
	v_mfma_f32_16x16x32_bf16 v[84:87], v[158:161], v[246:249], v[84:87]
	v_mfma_f32_16x16x32_bf16 v[76:79], v[166:169], v[246:249], v[76:79]
	s_setprio 0
	s_setprio 1
	v_mfma_f32_16x16x32_bf16 v[120:123], v[170:173], v[186:189], v[120:123]
	v_mfma_f32_16x16x32_bf16 v[112:115], v[178:181], v[186:189], v[112:115]
	v_mfma_f32_16x16x32_bf16 v[104:107], v[170:173], v[194:197], v[104:107]
	v_mfma_f32_16x16x32_bf16 v[96:99], v[178:181], v[194:197], v[96:99]
	v_mfma_f32_16x16x32_bf16 v[88:91], v[170:173], v[228:231], v[88:91]
	v_mfma_f32_16x16x32_bf16 v[80:83], v[178:181], v[228:231], v[80:83]
	v_mfma_f32_16x16x32_bf16 v[72:75], v[170:173], v[242:245], v[72:75]
	v_mfma_f32_16x16x32_bf16 v[68:71], v[178:181], v[242:245], v[68:71]
	v_mfma_f32_16x16x32_bf16 v[120:123], v[174:177], v[190:193], v[120:123]
	v_mfma_f32_16x16x32_bf16 v[112:115], v[182:185], v[190:193], v[112:115]
	v_mfma_f32_16x16x32_bf16 v[104:107], v[174:177], v[224:227], v[104:107]
	v_mfma_f32_16x16x32_bf16 v[96:99], v[182:185], v[224:227], v[96:99]
	v_mfma_f32_16x16x32_bf16 v[88:91], v[174:177], v[238:241], v[88:91]
	v_mfma_f32_16x16x32_bf16 v[80:83], v[182:185], v[238:241], v[80:83]
	v_mfma_f32_16x16x32_bf16 v[72:75], v[174:177], v[246:249], v[72:75]
	v_mfma_f32_16x16x32_bf16 v[68:71], v[182:185], v[246:249], v[68:71]
	s_setprio 0
	s_barrier
	s_add_i32 s4, s53, s14
	v_lshl_add_u64 v[148:149], v[148:149], 0, s[78:79]
	s_mov_b32 m0, s4
	s_nop 0
	global_load_lds_dwordx4 v[148:149], off
	s_add_i32 m0, s4, 0x2000
	s_add_u32 s4, s36, 0x20080
	v_lshl_add_u64 v[148:149], v[198:199], 0, s[78:79]
	s_addc_u32 s5, s37, 0
	s_add_i32 s36, s54, s14
	global_load_lds_dwordx4 v[148:149], off
	v_lshl_add_u64 v[148:149], s[4:5], 0, v[138:139]
	s_mov_b32 m0, s36
	s_nop 0
	global_load_lds_dwordx4 v[148:149], off
	v_lshl_add_u64 v[148:149], s[4:5], 0, v[132:133]
	s_add_i32 m0, s36, 0x2000
	s_nop 0
	global_load_lds_dwordx4 v[148:149], off
	v_lshl_add_u64 v[148:149], v[208:209], 0, s[78:79]
	s_mov_b32 m0, s45
	s_nop 0
	global_load_lds_dwordx4 v[148:149], off
	v_lshl_add_u64 v[148:149], v[212:213], 0, s[78:79]
	s_mov_b32 m0, s46
	s_nop 0
	global_load_lds_dwordx4 v[148:149], off
	ds_read_b128 v[186:189], v152 offset:49152
	ds_read_b128 v[190:193], v152 offset:50176
	ds_read_b128 v[194:197], v152 offset:51200
	ds_read_b128 v[224:227], v152 offset:52224
	ds_read_b128 v[228:231], v152 offset:53248
	ds_read_b128 v[238:241], v152 offset:54272
	ds_read_b128 v[242:245], v152 offset:55296
	ds_read_b128 v[246:249], v152 offset:56320
	s_waitcnt vmcnt(8)
	s_waitcnt lgkmcnt(0)
	s_barrier
	s_setprio 1
	s_waitcnt lgkmcnt(0)
	v_mfma_f32_16x16x32_bf16 v[64:67], v[154:157], v[186:189], v[64:67]
	v_mfma_f32_16x16x32_bf16 v[60:63], v[162:165], v[186:189], v[60:63]
	v_mfma_f32_16x16x32_bf16 v[52:55], v[154:157], v[194:197], v[52:55]
	v_mfma_f32_16x16x32_bf16 v[44:47], v[162:165], v[194:197], v[44:47]
	v_mfma_f32_16x16x32_bf16 v[36:39], v[154:157], v[228:231], v[36:39]
	v_mfma_f32_16x16x32_bf16 v[26:29], v[162:165], v[228:231], v[26:29]
	v_mfma_f32_16x16x32_bf16 v[18:21], v[154:157], v[242:245], v[18:21]
	v_mfma_f32_16x16x32_bf16 v[10:13], v[162:165], v[242:245], v[10:13]
	v_mfma_f32_16x16x32_bf16 v[64:67], v[158:161], v[190:193], v[64:67]
	v_mfma_f32_16x16x32_bf16 v[60:63], v[166:169], v[190:193], v[60:63]
	v_mfma_f32_16x16x32_bf16 v[52:55], v[158:161], v[224:227], v[52:55]
	v_mfma_f32_16x16x32_bf16 v[44:47], v[166:169], v[224:227], v[44:47]
	v_mfma_f32_16x16x32_bf16 v[36:39], v[158:161], v[238:241], v[36:39]
	v_mfma_f32_16x16x32_bf16 v[26:29], v[166:169], v[238:241], v[26:29]
	v_mfma_f32_16x16x32_bf16 v[18:21], v[158:161], v[246:249], v[18:21]
	v_mfma_f32_16x16x32_bf16 v[10:13], v[166:169], v[246:249], v[10:13]
	s_setprio 0
	s_setprio 1
	v_mfma_f32_16x16x32_bf16 v[56:59], v[170:173], v[186:189], v[56:59]
	v_mfma_f32_16x16x32_bf16 v[48:51], v[178:181], v[186:189], v[48:51]
	v_mfma_f32_16x16x32_bf16 v[40:43], v[170:173], v[194:197], v[40:43]
	v_mfma_f32_16x16x32_bf16 v[30:33], v[178:181], v[194:197], v[30:33]
	v_mfma_f32_16x16x32_bf16 v[22:25], v[170:173], v[228:231], v[22:25]
	v_mfma_f32_16x16x32_bf16 v[14:17], v[178:181], v[228:231], v[14:17]
	v_mfma_f32_16x16x32_bf16 v[6:9], v[170:173], v[242:245], v[6:9]
	v_mfma_f32_16x16x32_bf16 v[2:5], v[178:181], v[242:245], v[2:5]
	v_mfma_f32_16x16x32_bf16 v[56:59], v[174:177], v[190:193], v[56:59]
	v_mfma_f32_16x16x32_bf16 v[48:51], v[182:185], v[190:193], v[48:51]
	v_mfma_f32_16x16x32_bf16 v[40:43], v[174:177], v[224:227], v[40:43]
	v_mfma_f32_16x16x32_bf16 v[30:33], v[182:185], v[224:227], v[30:33]
	v_mfma_f32_16x16x32_bf16 v[22:25], v[174:177], v[238:241], v[22:25]
	v_mfma_f32_16x16x32_bf16 v[14:17], v[182:185], v[238:241], v[14:17]
	v_mfma_f32_16x16x32_bf16 v[6:9], v[174:177], v[246:249], v[6:9]
	v_mfma_f32_16x16x32_bf16 v[2:5], v[182:185], v[246:249], v[2:5]
	s_setprio 0
	s_barrier
	s_add_i32 s52, s52, 2
	s_add_u32 s50, s50, 0x100
	s_addc_u32 s51, s51, 0
	s_add_u32 s34, s34, 0x100
	s_addc_u32 s35, s35, 0
	s_cmp_gt_u32 s52, 5
	s_cbranch_scc0 .LBB0_1199
	s_and_b64 vcc, exec, s[22:23]
	s_cbranch_vccz .LBB0_1202
	s_barrier
